# v32 + epilogue lane-pair exchange by v_permlane16_swap instead of ds_bpermute (MoE gate/up + down epilogues, phase-2 epilogue)
# speedup vs baseline: 1.0309x; 1.0035x over previous
.LBB0_237:
	v_and_b32_e32 v131, 16, v132
	v_add_u32_e32 v133, 12, v130
	v_cmp_eq_u32_e32 vcc, 0, v131
	s_add_i32 s68, s68, s3
	v_and_or_b32 v132, v132, 15, s68
	v_cndmask_b32_e32 v130, v133, v130, vcc
	v_cvt_pk_bf16_f32 v133, v122, v123
	v_cvt_pk_bf16_f32 v125, v124, v125
	v_cvt_pk_bf16_f32 v126, v126, v127
	v_cvt_pk_bf16_f32 v127, v128, v129
	v_and_b32_e32 v128, 64, v1
	v_xor_b32_e32 v124, 16, v1
	v_add_u32_e32 v128, 64, v128
	v_cmp_lt_i32_e64 s[6:7], v124, v128
	v_cndmask_b32_e32 v122, v133, v126, vcc
	v_cndmask_b32_e32 v123, v125, v127, vcc
	v_cndmask_b32_e64 v124, v1, v124, s[6:7]
	v_lshlrev_b32_e32 v124, 2, v124
	s_nop 1
	v_permlane16_swap_b32_e32 v133, v126
	v_permlane16_swap_b32_e32 v125, v127
	v_mov_b64_e32 v[134:135], s[14:15]
	v_add_u32_e32 v130, s34, v130
	v_mad_u64_u32 v[122:123], s[6:7], v132, s58, v[134:135]
	v_cmp_gt_i32_e64 s[6:7], s61, v130
	v_ashrrev_i32_e32 v131, 31, v130
	s_and_saveexec_b64 s[8:9], s[6:7]
	s_cbranch_execz .LBB0_239
	v_lshl_add_u64 v[138:139], v[130:131], 1, v[122:123]
	s_waitcnt lgkmcnt(1)
	v_mov_b32_e32 v134, v133
	s_waitcnt lgkmcnt(0)
	v_mov_b32_e32 v135, v125
	v_mov_b32_e32 v136, v126
	v_mov_b32_e32 v137, v127
	global_store_dwordx4 v[138:139], v[134:137], off
.LBB0_239:
	s_or_b64 exec, exec, s[8:9]
	v_cvt_pk_bf16_f32 v114, v114, v115
	v_cvt_pk_bf16_f32 v115, v116, v117
	v_cvt_pk_bf16_f32 v110, v110, v111
	v_cvt_pk_bf16_f32 v111, v112, v113
	v_add_u32_e32 v116, 32, v130
	v_cndmask_b32_e32 v112, v114, v110, vcc
	v_cndmask_b32_e32 v113, v115, v111, vcc
	s_nop 1
	v_permlane16_swap_b32_e32 v114, v110
	v_permlane16_swap_b32_e32 v115, v111
	v_cmp_gt_i32_e64 s[8:9], s61, v116
	s_and_saveexec_b64 s[34:35], s[8:9]
	s_cbranch_execz .LBB0_241
	v_lshl_add_u64 v[122:123], v[130:131], 1, v[122:123]
	s_waitcnt lgkmcnt(1)
	s_waitcnt lgkmcnt(0)
	v_mov_b32_e32 v116, v110
	v_mov_b32_e32 v117, v111
	global_store_dwordx4 v[122:123], v[114:117], off offset:64
.LBB0_241:
	s_or_b64 exec, exec, s[34:35]
	v_cvt_pk_bf16_f32 v110, v106, v107
	v_cvt_pk_bf16_f32 v108, v108, v109
	v_cvt_pk_bf16_f32 v109, v118, v119
	v_cvt_pk_bf16_f32 v111, v120, v121
	s_nop 0
	v_or_b32_e32 v114, 16, v132
	v_cndmask_b32_e32 v106, v110, v109, vcc
	v_cndmask_b32_e32 v107, v108, v111, vcc
	s_waitcnt lgkmcnt(1)
	s_nop 1
	v_permlane16_swap_b32_e32 v110, v109
	s_waitcnt lgkmcnt(1)
	v_permlane16_swap_b32_e32 v108, v111
	v_mov_b64_e32 v[106:107], s[14:15]
	v_mad_u64_u32 v[106:107], s[34:35], v114, s58, v[106:107]
	s_and_saveexec_b64 s[34:35], s[6:7]
	s_cbranch_execz .LBB0_243
	v_lshl_add_u64 v[118:119], v[130:131], 1, v[106:107]
	s_waitcnt lgkmcnt(1)
	v_mov_b32_e32 v114, v110
	s_waitcnt lgkmcnt(0)
	v_mov_b32_e32 v115, v108
	v_mov_b32_e32 v116, v109
	v_mov_b32_e32 v117, v111
	global_store_dwordx4 v[118:119], v[114:117], off
.LBB0_243:
	s_or_b64 exec, exec, s[34:35]
	v_cvt_pk_bf16_f32 v98, v98, v99
	v_cvt_pk_bf16_f32 v99, v100, v101
	v_cvt_pk_bf16_f32 v94, v94, v95
	v_cvt_pk_bf16_f32 v95, v96, v97
	s_nop 0
	v_cndmask_b32_e32 v96, v98, v94, vcc
	v_cndmask_b32_e32 v97, v99, v95, vcc
	s_nop 1
	v_permlane16_swap_b32_e32 v98, v94
	v_permlane16_swap_b32_e32 v99, v95
	s_and_saveexec_b64 s[34:35], s[8:9]
	s_cbranch_execz .LBB0_245
	v_lshl_add_u64 v[106:107], v[130:131], 1, v[106:107]
	s_waitcnt lgkmcnt(1)
	s_waitcnt lgkmcnt(0)
	v_mov_b32_e32 v100, v94
	v_mov_b32_e32 v101, v95
	global_store_dwordx4 v[106:107], v[98:101], off offset:64
.LBB0_245:
	s_or_b64 exec, exec, s[34:35]
	v_cvt_pk_bf16_f32 v94, v90, v91
	v_cvt_pk_bf16_f32 v92, v92, v93
	v_cvt_pk_bf16_f32 v93, v102, v103
	v_cvt_pk_bf16_f32 v95, v104, v105
	s_nop 0
	v_or_b32_e32 v98, 32, v132
	v_cndmask_b32_e32 v90, v94, v93, vcc
	v_cndmask_b32_e32 v91, v92, v95, vcc
	s_waitcnt lgkmcnt(1)
	s_nop 1
	v_permlane16_swap_b32_e32 v94, v93
	s_waitcnt lgkmcnt(1)
	v_permlane16_swap_b32_e32 v92, v95
	v_mov_b64_e32 v[90:91], s[14:15]
	v_mad_u64_u32 v[90:91], s[34:35], v98, s58, v[90:91]
	s_and_saveexec_b64 s[34:35], s[6:7]
	s_cbranch_execz .LBB0_247
	v_lshl_add_u64 v[102:103], v[130:131], 1, v[90:91]
	s_waitcnt lgkmcnt(1)
	v_mov_b32_e32 v98, v94
	s_waitcnt lgkmcnt(0)
	v_mov_b32_e32 v99, v92
	v_mov_b32_e32 v100, v93
	v_mov_b32_e32 v101, v95
	global_store_dwordx4 v[102:103], v[98:101], off
.LBB0_247:
	s_or_b64 exec, exec, s[34:35]
	v_cvt_pk_bf16_f32 v82, v82, v83
	v_cvt_pk_bf16_f32 v83, v84, v85
	v_cvt_pk_bf16_f32 v78, v78, v79
	v_cvt_pk_bf16_f32 v79, v80, v81
	s_nop 0
	v_cndmask_b32_e32 v80, v82, v78, vcc
	v_cndmask_b32_e32 v81, v83, v79, vcc
	s_nop 1
	v_permlane16_swap_b32_e32 v82, v78
	v_permlane16_swap_b32_e32 v83, v79
	s_and_saveexec_b64 s[34:35], s[8:9]
	s_cbranch_execz .LBB0_249
	v_lshl_add_u64 v[90:91], v[130:131], 1, v[90:91]
	s_waitcnt lgkmcnt(1)
	s_waitcnt lgkmcnt(0)
	v_mov_b32_e32 v84, v78
	v_mov_b32_e32 v85, v79
	global_store_dwordx4 v[90:91], v[82:85], off offset:64
.LBB0_249:
	s_or_b64 exec, exec, s[34:35]
	v_cvt_pk_bf16_f32 v78, v74, v75
	v_cvt_pk_bf16_f32 v76, v76, v77
	v_cvt_pk_bf16_f32 v77, v86, v87
	v_cvt_pk_bf16_f32 v79, v88, v89
	s_nop 0
	v_or_b32_e32 v82, 48, v132
	v_cndmask_b32_e32 v74, v78, v77, vcc
	v_cndmask_b32_e32 v75, v76, v79, vcc
	s_waitcnt lgkmcnt(1)
	s_nop 1
	v_permlane16_swap_b32_e32 v78, v77
	s_waitcnt lgkmcnt(1)
	v_permlane16_swap_b32_e32 v76, v79
	v_mov_b64_e32 v[74:75], s[14:15]
	v_mad_u64_u32 v[74:75], s[34:35], v82, s58, v[74:75]
	s_and_saveexec_b64 s[34:35], s[6:7]
	s_cbranch_execz .LBB0_251
	v_lshl_add_u64 v[86:87], v[130:131], 1, v[74:75]
	s_waitcnt lgkmcnt(1)
	v_mov_b32_e32 v82, v78
	s_waitcnt lgkmcnt(0)
	v_mov_b32_e32 v83, v76
	v_mov_b32_e32 v84, v77
	v_mov_b32_e32 v85, v79
	global_store_dwordx4 v[86:87], v[82:85], off
.LBB0_251:
	s_or_b64 exec, exec, s[34:35]
	v_cvt_pk_bf16_f32 v70, v70, v71
	v_cvt_pk_bf16_f32 v71, v72, v73
	v_cvt_pk_bf16_f32 v62, v62, v63
	v_cvt_pk_bf16_f32 v63, v64, v65
	s_nop 0
	v_cndmask_b32_e32 v64, v70, v62, vcc
	v_cndmask_b32_e32 v65, v71, v63, vcc
	s_nop 1
	v_permlane16_swap_b32_e32 v70, v62
	v_permlane16_swap_b32_e32 v71, v63
	s_and_saveexec_b64 s[34:35], s[8:9]
	s_cbranch_execz .LBB0_253
	v_lshl_add_u64 v[74:75], v[130:131], 1, v[74:75]
	s_waitcnt lgkmcnt(1)
	s_waitcnt lgkmcnt(0)
	v_mov_b32_e32 v72, v62
	v_mov_b32_e32 v73, v63
	global_store_dwordx4 v[74:75], v[70:73], off offset:64
.LBB0_253:
	s_or_b64 exec, exec, s[34:35]
	v_cvt_pk_bf16_f32 v62, v58, v59
	v_cvt_pk_bf16_f32 v60, v60, v61
	v_cvt_pk_bf16_f32 v61, v66, v67
	v_cvt_pk_bf16_f32 v63, v68, v69
	v_or_b32_e32 v66, 64, v132
	v_cndmask_b32_e32 v58, v62, v61, vcc
	v_cndmask_b32_e32 v59, v60, v63, vcc
	s_waitcnt lgkmcnt(1)
	s_nop 1
	v_permlane16_swap_b32_e32 v62, v61
	s_waitcnt lgkmcnt(1)
	v_permlane16_swap_b32_e32 v60, v63
	v_mov_b64_e32 v[58:59], s[14:15]
	v_mad_u64_u32 v[58:59], s[34:35], v66, s58, v[58:59]
	s_and_saveexec_b64 s[34:35], s[6:7]
	s_cbranch_execz .LBB0_255
	v_lshl_add_u64 v[70:71], v[130:131], 1, v[58:59]
	s_waitcnt lgkmcnt(1)
	v_mov_b32_e32 v66, v62
	s_waitcnt lgkmcnt(0)
	v_mov_b32_e32 v67, v60
	v_mov_b32_e32 v68, v61
	v_mov_b32_e32 v69, v63
	global_store_dwordx4 v[70:71], v[66:69], off
.LBB0_255:
	s_or_b64 exec, exec, s[34:35]
	v_cvt_pk_bf16_f32 v54, v54, v55
	v_cvt_pk_bf16_f32 v55, v56, v57
	v_cvt_pk_bf16_f32 v46, v46, v47
	v_cvt_pk_bf16_f32 v47, v48, v49
	s_nop 0
	v_cndmask_b32_e32 v48, v54, v46, vcc
	v_cndmask_b32_e32 v49, v55, v47, vcc
	s_nop 1
	v_permlane16_swap_b32_e32 v54, v46
	v_permlane16_swap_b32_e32 v55, v47
	s_and_saveexec_b64 s[34:35], s[8:9]
	s_cbranch_execz .LBB0_257
	v_lshl_add_u64 v[58:59], v[130:131], 1, v[58:59]
	s_waitcnt lgkmcnt(1)
	s_waitcnt lgkmcnt(0)
	v_mov_b32_e32 v56, v46
	v_mov_b32_e32 v57, v47
	global_store_dwordx4 v[58:59], v[54:57], off offset:64
.LBB0_257:
	s_or_b64 exec, exec, s[34:35]
	v_cvt_pk_bf16_f32 v46, v42, v43
	v_cvt_pk_bf16_f32 v44, v44, v45
	v_cvt_pk_bf16_f32 v45, v50, v51
	v_cvt_pk_bf16_f32 v47, v52, v53
	v_or_b32_e32 v50, 0x50, v132
	v_cndmask_b32_e32 v42, v46, v45, vcc
	v_cndmask_b32_e32 v43, v44, v47, vcc
	s_waitcnt lgkmcnt(1)
	s_nop 1
	v_permlane16_swap_b32_e32 v46, v45
	s_waitcnt lgkmcnt(1)
	v_permlane16_swap_b32_e32 v44, v47
	v_mov_b64_e32 v[42:43], s[14:15]
	v_mad_u64_u32 v[42:43], s[34:35], v50, s58, v[42:43]
	s_and_saveexec_b64 s[34:35], s[6:7]
	s_cbranch_execz .LBB0_259
	v_lshl_add_u64 v[54:55], v[130:131], 1, v[42:43]
	s_waitcnt lgkmcnt(1)
	v_mov_b32_e32 v50, v46
	s_waitcnt lgkmcnt(0)
	v_mov_b32_e32 v51, v44
	v_mov_b32_e32 v52, v45
	v_mov_b32_e32 v53, v47
	global_store_dwordx4 v[54:55], v[50:53], off
.LBB0_259:
	s_or_b64 exec, exec, s[34:35]
	v_cvt_pk_bf16_f32 v38, v38, v39
	v_cvt_pk_bf16_f32 v39, v40, v41
	v_cvt_pk_bf16_f32 v34, v34, v35
	v_cvt_pk_bf16_f32 v35, v36, v37
	s_nop 0
	v_cndmask_b32_e32 v36, v38, v34, vcc
	v_cndmask_b32_e32 v37, v39, v35, vcc
	s_nop 1
	v_permlane16_swap_b32_e32 v38, v34
	v_permlane16_swap_b32_e32 v39, v35
	s_and_saveexec_b64 s[34:35], s[8:9]
	s_cbranch_execz .LBB0_261
	v_lshl_add_u64 v[42:43], v[130:131], 1, v[42:43]
	s_waitcnt lgkmcnt(1)
	s_waitcnt lgkmcnt(0)
	v_mov_b32_e32 v40, v34
	v_mov_b32_e32 v41, v35
	global_store_dwordx4 v[42:43], v[38:41], off offset:64
.LBB0_261:
	s_or_b64 exec, exec, s[34:35]
	v_cvt_pk_bf16_f32 v34, v26, v27
	v_cvt_pk_bf16_f32 v28, v28, v29
	v_cvt_pk_bf16_f32 v29, v30, v31
	v_cvt_pk_bf16_f32 v30, v32, v33
	v_or_b32_e32 v33, 0x60, v132
	v_cndmask_b32_e32 v26, v34, v29, vcc
	v_cndmask_b32_e32 v27, v28, v30, vcc
	s_nop 1
	v_permlane16_swap_b32_e32 v34, v29
	v_permlane16_swap_b32_e32 v28, v30
	v_mov_b64_e32 v[26:27], s[14:15]
	v_mad_u64_u32 v[26:27], s[34:35], v33, s58, v[26:27]
	s_and_saveexec_b64 s[34:35], s[6:7]
	s_cbranch_execz .LBB0_263
	v_lshl_add_u64 v[38:39], v[130:131], 1, v[26:27]
	s_waitcnt lgkmcnt(1)
	s_waitcnt lgkmcnt(0)
	v_mov_b32_e32 v35, v28
	v_mov_b32_e32 v36, v29
	v_mov_b32_e32 v37, v30
	global_store_dwordx4 v[38:39], v[34:37], off
.LBB0_263:
	s_or_b64 exec, exec, s[34:35]
	v_cvt_pk_bf16_f32 v22, v22, v23
	v_cvt_pk_bf16_f32 v23, v24, v25
	v_cvt_pk_bf16_f32 v18, v18, v19
	v_cvt_pk_bf16_f32 v19, v20, v21
	s_nop 0
	v_cndmask_b32_e32 v20, v22, v18, vcc
	v_cndmask_b32_e32 v21, v23, v19, vcc
	s_nop 1
	v_permlane16_swap_b32_e32 v22, v18
	v_permlane16_swap_b32_e32 v23, v19
	s_and_saveexec_b64 s[34:35], s[8:9]
	s_cbranch_execz .LBB0_265
	v_lshl_add_u64 v[26:27], v[130:131], 1, v[26:27]
	s_waitcnt lgkmcnt(1)
	s_waitcnt lgkmcnt(0)
	v_mov_b32_e32 v24, v18
	v_mov_b32_e32 v25, v19
	global_store_dwordx4 v[26:27], v[22:25], off offset:64
.LBB0_265:
	s_or_b64 exec, exec, s[34:35]
	v_cvt_pk_bf16_f32 v18, v10, v11
	v_cvt_pk_bf16_f32 v12, v12, v13
	v_cvt_pk_bf16_f32 v13, v14, v15
	v_cvt_pk_bf16_f32 v14, v16, v17
	v_or_b32_e32 v17, 0x70, v132
	v_cndmask_b32_e32 v10, v18, v13, vcc
	v_cndmask_b32_e32 v11, v12, v14, vcc
	s_nop 1
	v_permlane16_swap_b32_e32 v18, v13
	v_permlane16_swap_b32_e32 v12, v14
	v_mov_b64_e32 v[10:11], s[14:15]
	v_mad_u64_u32 v[10:11], s[34:35], v17, s58, v[10:11]
	s_and_saveexec_b64 s[34:35], s[6:7]
	s_cbranch_execz .LBB0_267
	v_lshl_add_u64 v[22:23], v[130:131], 1, v[10:11]
	s_waitcnt lgkmcnt(1)
	s_waitcnt lgkmcnt(0)
	v_mov_b32_e32 v19, v12
	v_mov_b32_e32 v20, v13
	v_mov_b32_e32 v21, v14
	global_store_dwordx4 v[22:23], v[18:21], off
.LBB0_267:
	s_or_b64 exec, exec, s[34:35]
	v_cvt_pk_bf16_f32 v6, v6, v7
	v_cvt_pk_bf16_f32 v7, v8, v9
	v_cvt_pk_bf16_f32 v2, v2, v3
	v_cvt_pk_bf16_f32 v3, v4, v5
	s_nop 0
	v_cndmask_b32_e32 v4, v6, v2, vcc
	v_cndmask_b32_e32 v5, v7, v3, vcc
	s_nop 1
	v_permlane16_swap_b32_e32 v6, v2
	v_permlane16_swap_b32_e32 v7, v3
	s_and_saveexec_b64 s[6:7], s[8:9]
	s_cbranch_execz .LBB0_204
	v_lshl_add_u64 v[10:11], v[130:131], 1, v[10:11]
	s_waitcnt lgkmcnt(1)
	s_waitcnt lgkmcnt(0)
	v_mov_b32_e32 v8, v2
	v_mov_b32_e32 v9, v3
	global_store_dwordx4 v[10:11], v[6:9], off offset:64
	s_branch .LBB0_204

.LBB0_1277:
	s_lshl_b32 s10, s48, 11
	s_ashr_i32 s11, s10, 31
	s_lshl_b32 s2, s34, 6
	s_lshl_b64 s[10:11], s[10:11], 2
	s_add_u32 s33, s20, s10
	s_addc_u32 s35, s21, s11
	s_ashr_i32 s47, s46, 31
	s_lshl_b64 s[10:11], s[46:47], 2
	s_add_u32 s10, s33, s10
	s_addc_u32 s11, s35, s11
	s_lshl_b32 s33, s34, 8
	s_add_u32 s10, s10, s33
	s_addc_u32 s11, s11, 0
	v_ashrrev_i32_e32 v5, 31, v4
	v_lshl_add_u64 v[150:151], v[4:5], 2, s[10:11]
	s_add_i32 s10, s5, s4
	v_and_or_b32 v1, v3, 15, s10
	s_add_i32 s10, s86, -1
	s_lshl_b32 s11, s48, 13
	v_min_i32_e32 v5, s10, v1
	v_add_u32_e32 v166, s11, v5
	v_ashrrev_i32_e32 v167, 31, v166
	v_or_b32_e32 v193, 16, v1
	v_lshl_add_u64 v[166:167], v[166:167], 2, s[56:57]
	v_min_i32_e32 v5, s10, v193
	global_load_dwordx4 v[162:165], v[150:151], off
	global_load_dwordx4 v[158:161], v[150:151], off offset:64
	global_load_dwordx4 v[154:157], v[150:151], off offset:128
	s_nop 0
	global_load_dwordx4 v[150:153], v[150:151], off offset:192
	v_or_b32_e32 v189, 32, v1
	global_load_dword v204, v[166:167], off
	v_add_u32_e32 v166, s11, v5
	v_ashrrev_i32_e32 v167, 31, v166
	v_lshl_add_u64 v[166:167], v[166:167], 2, s[56:57]
	global_load_dword v190, v[166:167], off
	v_min_i32_e32 v5, s10, v189
	v_or_b32_e32 v185, 48, v1
	v_or_b32_e32 v179, 64, v1
	v_or_b32_e32 v175, 0x50, v1
	v_or_b32_e32 v171, 0x60, v1
	v_xor_b32_e32 v209, 16, v206
	v_cmp_gt_i32_e32 vcc, s86, v1
	s_add_i32 s2, s2, s46
	s_waitcnt vmcnt(5)
	v_pk_add_f32 v[214:215], v[148:149], v[164:165]
	v_pk_add_f32 v[216:217], v[146:147], v[162:163]
	s_waitcnt vmcnt(1)
	v_ashrrev_i32_e32 v205, 31, v204
	v_lshl_add_u64 v[168:169], v[204:205], 2, s[58:59]
	global_load_dword v196, v[168:169], off
	v_add_u32_e32 v166, s11, v5
	s_waitcnt vmcnt(1)
	v_ashrrev_i32_e32 v191, 31, v190
	v_ashrrev_i32_e32 v167, 31, v166
	v_lshl_add_u64 v[166:167], v[166:167], 2, s[56:57]
	v_min_i32_e32 v5, s10, v185
	v_lshl_add_u64 v[168:169], v[190:191], 2, s[58:59]
	global_load_dword v186, v[166:167], off
	global_load_dword v194, v[168:169], off
	v_add_u32_e32 v166, s11, v5
	v_ashrrev_i32_e32 v167, 31, v166
	v_lshl_add_u64 v[166:167], v[166:167], 2, s[56:57]
	global_load_dword v182, v[166:167], off
	v_min_i32_e32 v5, s10, v179
	v_lshlrev_b64 v[204:205], 12, v[204:205]
	v_lshl_add_u64 v[204:205], s[60:61], 0, v[204:205]
	s_waitcnt vmcnt(3)
	v_pk_mul_f32 v[214:215], v[214:215], v[196:197] op_sel_hi:[1,0]
	v_pk_mul_f32 v[216:217], v[216:217], v[196:197] op_sel_hi:[1,0]
	s_waitcnt vmcnt(2)
	v_ashrrev_i32_e32 v187, 31, v186
	v_lshl_add_u64 v[168:169], v[186:187], 2, s[58:59]
	global_load_dword v192, v[168:169], off
	v_add_u32_e32 v166, s11, v5
	v_ashrrev_i32_e32 v167, 31, v166
	s_waitcnt vmcnt(1)
	v_ashrrev_i32_e32 v183, 31, v182
	v_lshl_add_u64 v[166:167], v[166:167], 2, s[56:57]
	v_min_i32_e32 v5, s10, v175
	v_lshl_add_u64 v[168:169], v[182:183], 2, s[58:59]
	global_load_dword v180, v[166:167], off
	global_load_dword v188, v[168:169], off
	v_add_u32_e32 v166, s11, v5
	v_ashrrev_i32_e32 v167, 31, v166
	v_lshl_add_u64 v[166:167], v[166:167], 2, s[56:57]
	global_load_dword v176, v[166:167], off
	v_min_i32_e32 v5, s10, v171
	s_waitcnt vmcnt(2)
	v_ashrrev_i32_e32 v181, 31, v180
	v_lshl_add_u64 v[168:169], v[180:181], 2, s[58:59]
	global_load_dword v184, v[168:169], off
	v_add_u32_e32 v166, s11, v5
	v_ashrrev_i32_e32 v167, 31, v166
	s_waitcnt vmcnt(1)
	v_ashrrev_i32_e32 v177, 31, v176
	v_lshl_add_u64 v[166:167], v[166:167], 2, s[56:57]
	v_or_b32_e32 v5, 0x70, v1
	v_lshl_add_u64 v[168:169], v[176:177], 2, s[58:59]
	global_load_dword v172, v[166:167], off
	global_load_dword v178, v[168:169], off
	v_min_i32_e32 v166, s10, v5
	v_add_u32_e32 v166, s11, v166
	v_ashrrev_i32_e32 v167, 31, v166
	v_lshl_add_u64 v[166:167], v[166:167], 2, s[56:57]
	global_load_dword v166, v[166:167], off
	s_waitcnt vmcnt(2)
	v_ashrrev_i32_e32 v173, 31, v172
	v_lshl_add_u64 v[168:169], v[172:173], 2, s[58:59]
	global_load_dword v174, v[168:169], off
	s_waitcnt vmcnt(1)
	v_ashrrev_i32_e32 v167, 31, v166
	v_lshl_add_u64 v[168:169], v[166:167], 2, s[58:59]
	global_load_dword v170, v[168:169], off
	v_cvt_pk_bf16_f32 v195, v216, v217
	v_cvt_pk_bf16_f32 v197, v214, v215
	v_pk_add_f32 v[214:215], v[144:145], v[160:161]
	v_pk_add_f32 v[216:217], v[142:143], v[158:159]
	v_pk_mul_f32 v[214:215], v[214:215], v[196:197] op_sel_hi:[1,0]
	v_pk_mul_f32 v[216:217], v[216:217], v[196:197] op_sel_hi:[1,0]
	v_cndmask_b32_e64 v168, v208, v4, s[8:9]
	v_cvt_pk_bf16_f32 v213, v216, v217
	v_cvt_pk_bf16_f32 v214, v214, v215
	v_and_b32_e32 v215, 64, v206
	v_add_u32_e32 v215, 64, v215
	v_cmp_lt_i32_e64 s[10:11], v209, v215
	v_cndmask_b32_e64 v1, v195, v213, s[8:9]
	v_cndmask_b32_e64 v169, v197, v214, s[8:9]
	v_cndmask_b32_e64 v209, v206, v209, s[10:11]
	v_lshlrev_b32_e32 v209, 2, v209
	s_nop 1
	v_permlane16_swap_b32_e32 v195, v213
	v_permlane16_swap_b32_e32 v197, v214
	v_add_u32_e32 v168, s2, v168
	v_ashrrev_i32_e32 v169, 31, v168
	s_and_saveexec_b64 s[10:11], vcc
	s_cbranch_execz .LBB0_1279
	s_waitcnt lgkmcnt(1)
	v_mov_b32_e32 v218, v195
	s_waitcnt lgkmcnt(0)
	v_mov_b32_e32 v219, v197
	v_mov_b32_e32 v220, v213
	v_mov_b32_e32 v221, v214
	v_lshl_add_u64 v[214:215], v[168:169], 1, v[204:205]
	global_store_dwordx4 v[214:215], v[218:221], off
.LBB0_1279:
	s_or_b64 exec, exec, s[10:11]
	v_mov_b32_e32 v197, v196
	s_waitcnt lgkmcnt(1)
	v_pk_add_f32 v[214:215], v[140:141], v[156:157]
	s_waitcnt lgkmcnt(0)
	v_pk_add_f32 v[216:217], v[138:139], v[154:155]
	v_mov_b32_e32 v218, v196
	v_mov_b32_e32 v219, v196
	v_pk_mul_f32 v[214:215], v[214:215], v[218:219]
	v_pk_mul_f32 v[216:217], v[216:217], v[196:197]
	s_nop 0
	v_cvt_pk_bf16_f32 v195, v216, v217
	v_cvt_pk_bf16_f32 v213, v214, v215
	v_pk_add_f32 v[214:215], v[136:137], v[152:153]
	v_pk_add_f32 v[216:217], v[134:135], v[150:151]
	v_pk_mul_f32 v[214:215], v[214:215], v[218:219]
	v_pk_mul_f32 v[196:197], v[216:217], v[196:197]
	s_nop 0
	v_cvt_pk_bf16_f32 v196, v196, v197
	v_cvt_pk_bf16_f32 v197, v214, v215
	s_nop 0
	v_cndmask_b32_e64 v1, v195, v196, s[8:9]
	v_cndmask_b32_e64 v215, v213, v197, s[8:9]
	s_nop 1
	v_permlane16_swap_b32_e32 v195, v196
	v_permlane16_swap_b32_e32 v213, v197
	s_and_saveexec_b64 s[10:11], vcc
	s_cbranch_execz .LBB0_1281
	s_waitcnt lgkmcnt(1)
	v_mov_b32_e32 v216, v195
	s_waitcnt lgkmcnt(0)
	v_mov_b32_e32 v217, v213
	v_mov_b32_e32 v218, v196
	v_mov_b32_e32 v219, v197
	v_lshl_add_u64 v[196:197], v[168:169], 1, v[204:205]
	global_store_dwordx4 v[196:197], v[216:219], off offset:64
.LBB0_1281:
	s_or_b64 exec, exec, s[10:11]
	v_pk_add_f32 v[204:205], v[130:131], v[162:163]
	v_pk_add_f32 v[196:197], v[132:133], v[164:165]
	v_pk_mul_f32 v[204:205], v[204:205], v[194:195] op_sel_hi:[1,0]
	v_pk_mul_f32 v[196:197], v[196:197], v[194:195] op_sel_hi:[1,0]
	v_cvt_pk_bf16_f32 v195, v204, v205
	v_pk_add_f32 v[204:205], v[124:125], v[160:161]
	s_waitcnt lgkmcnt(0)
	v_pk_add_f32 v[214:215], v[122:123], v[158:159]
	v_pk_mul_f32 v[204:205], v[204:205], v[194:195] op_sel_hi:[1,0]
	v_cvt_pk_bf16_f32 v196, v196, v197
	v_pk_mul_f32 v[214:215], v[214:215], v[194:195] op_sel_hi:[1,0]
	v_lshlrev_b64 v[190:191], 12, v[190:191]
	v_cvt_pk_bf16_f32 v197, v214, v215
	v_cvt_pk_bf16_f32 v204, v204, v205
	v_cmp_gt_i32_e32 vcc, s86, v193
	v_cndmask_b32_e64 v1, v195, v197, s[8:9]
	v_cndmask_b32_e64 v213, v196, v204, s[8:9]
	s_nop 1
	v_permlane16_swap_b32_e32 v195, v197
	v_permlane16_swap_b32_e32 v196, v204
	v_lshl_add_u64 v[190:191], s[60:61], 0, v[190:191]
	s_and_saveexec_b64 s[10:11], vcc
	s_cbranch_execz .LBB0_1283
	s_waitcnt lgkmcnt(1)
	v_mov_b32_e32 v214, v195
	s_waitcnt lgkmcnt(0)
	v_mov_b32_e32 v215, v196
	v_mov_b32_e32 v216, v197
	v_mov_b32_e32 v217, v204
	v_lshl_add_u64 v[196:197], v[168:169], 1, v[190:191]
	global_store_dwordx4 v[196:197], v[214:217], off
.LBB0_1283:
	s_or_b64 exec, exec, s[10:11]
	v_mov_b32_e32 v195, v194
	s_waitcnt lgkmcnt(1)
	v_pk_add_f32 v[204:205], v[126:127], v[154:155]
	v_pk_add_f32 v[196:197], v[128:129], v[156:157]
	v_pk_mul_f32 v[204:205], v[204:205], v[194:195]
	v_mov_b32_e32 v214, v194
	v_mov_b32_e32 v215, v194
	v_cvt_pk_bf16_f32 v193, v204, v205
	v_pk_add_f32 v[204:205], v[120:121], v[152:153]
	v_pk_add_f32 v[216:217], v[118:119], v[150:151]
	v_pk_mul_f32 v[196:197], v[196:197], v[214:215]
	v_pk_mul_f32 v[204:205], v[204:205], v[214:215]
	v_pk_mul_f32 v[194:195], v[216:217], v[194:195]
	v_cvt_pk_bf16_f32 v196, v196, v197
	s_nop 0
	v_cvt_pk_bf16_f32 v194, v194, v195
	v_cvt_pk_bf16_f32 v195, v204, v205
	s_nop 0
	v_cndmask_b32_e64 v1, v193, v194, s[8:9]
	v_cndmask_b32_e64 v204, v196, v195, s[8:9]
	s_nop 1
	v_permlane16_swap_b32_e32 v193, v194
	v_permlane16_swap_b32_e32 v196, v195
	s_and_saveexec_b64 s[10:11], vcc
	s_cbranch_execz .LBB0_1285
	s_waitcnt lgkmcnt(1)
	v_mov_b32_e32 v214, v193
	s_waitcnt lgkmcnt(0)
	v_mov_b32_e32 v215, v196
	v_mov_b32_e32 v216, v194
	v_mov_b32_e32 v217, v195
	v_lshl_add_u64 v[190:191], v[168:169], 1, v[190:191]
	global_store_dwordx4 v[190:191], v[214:217], off offset:64
.LBB0_1285:
	s_or_b64 exec, exec, s[10:11]
	v_pk_add_f32 v[190:191], v[116:117], v[164:165]
	v_pk_add_f32 v[194:195], v[114:115], v[162:163]
	s_waitcnt lgkmcnt(1)
	v_pk_mul_f32 v[196:197], v[190:191], v[192:193] op_sel_hi:[1,0]
	v_pk_mul_f32 v[190:191], v[194:195], v[192:193] op_sel_hi:[1,0]
	v_pk_add_f32 v[194:195], v[108:109], v[160:161]
	v_cvt_pk_bf16_f32 v190, v190, v191
	v_cvt_pk_bf16_f32 v191, v196, v197
	v_pk_add_f32 v[196:197], v[106:107], v[158:159]
	v_pk_mul_f32 v[194:195], v[194:195], v[192:193] op_sel_hi:[1,0]
	v_pk_mul_f32 v[196:197], v[196:197], v[192:193] op_sel_hi:[1,0]
	v_lshlrev_b64 v[186:187], 12, v[186:187]
	v_cvt_pk_bf16_f32 v193, v196, v197
	v_cvt_pk_bf16_f32 v194, v194, v195
	v_cmp_gt_i32_e32 vcc, s86, v189
	v_cndmask_b32_e64 v1, v190, v193, s[8:9]
	v_cndmask_b32_e64 v196, v191, v194, s[8:9]
	s_nop 1
	v_permlane16_swap_b32_e32 v190, v193
	v_permlane16_swap_b32_e32 v191, v194
	v_lshl_add_u64 v[186:187], s[60:61], 0, v[186:187]
	s_and_saveexec_b64 s[10:11], vcc
	s_cbranch_execz .LBB0_1287
	s_waitcnt lgkmcnt(1)
	v_mov_b32_e32 v214, v190
	s_waitcnt lgkmcnt(0)
	v_mov_b32_e32 v215, v191
	v_mov_b32_e32 v216, v193
	v_mov_b32_e32 v217, v194
	v_lshl_add_u64 v[190:191], v[168:169], 1, v[186:187]
	global_store_dwordx4 v[190:191], v[214:217], off
.LBB0_1287:
	s_or_b64 exec, exec, s[10:11]
	v_mov_b32_e32 v193, v192
	s_waitcnt lgkmcnt(1)
	v_pk_add_f32 v[194:195], v[110:111], v[154:155]
	v_pk_add_f32 v[190:191], v[112:113], v[156:157]
	v_pk_mul_f32 v[194:195], v[194:195], v[192:193]
	s_waitcnt lgkmcnt(0)
	v_mov_b32_e32 v196, v192
	v_mov_b32_e32 v197, v192
	v_cvt_pk_bf16_f32 v189, v194, v195
	v_pk_add_f32 v[194:195], v[104:105], v[152:153]
	v_pk_add_f32 v[204:205], v[102:103], v[150:151]
	v_pk_mul_f32 v[190:191], v[190:191], v[196:197]
	v_pk_mul_f32 v[194:195], v[194:195], v[196:197]
	v_pk_mul_f32 v[192:193], v[204:205], v[192:193]
	v_cvt_pk_bf16_f32 v190, v190, v191
	s_nop 0
	v_cvt_pk_bf16_f32 v191, v192, v193
	v_cvt_pk_bf16_f32 v192, v194, v195
	s_nop 0
	v_cndmask_b32_e64 v1, v189, v191, s[8:9]
	v_cndmask_b32_e64 v194, v190, v192, s[8:9]
	s_nop 1
	v_permlane16_swap_b32_e32 v189, v191
	v_permlane16_swap_b32_e32 v190, v192
	s_and_saveexec_b64 s[10:11], vcc
	s_cbranch_execz .LBB0_1289
	s_waitcnt lgkmcnt(1)
	v_mov_b32_e32 v214, v189
	s_waitcnt lgkmcnt(0)
	v_mov_b32_e32 v215, v190
	v_mov_b32_e32 v216, v191
	v_mov_b32_e32 v217, v192
	v_lshl_add_u64 v[186:187], v[168:169], 1, v[186:187]
	global_store_dwordx4 v[186:187], v[214:217], off offset:64
.LBB0_1289:
	s_or_b64 exec, exec, s[10:11]
	v_pk_add_f32 v[186:187], v[100:101], v[164:165]
	v_pk_add_f32 v[190:191], v[98:99], v[162:163]
	s_waitcnt lgkmcnt(1)
	v_pk_mul_f32 v[192:193], v[186:187], v[188:189] op_sel_hi:[1,0]
	v_pk_mul_f32 v[186:187], v[190:191], v[188:189] op_sel_hi:[1,0]
	v_pk_add_f32 v[190:191], v[92:93], v[160:161]
	v_cvt_pk_bf16_f32 v186, v186, v187
	v_cvt_pk_bf16_f32 v187, v192, v193
	v_pk_add_f32 v[192:193], v[90:91], v[158:159]
	v_pk_mul_f32 v[190:191], v[190:191], v[188:189] op_sel_hi:[1,0]
	v_pk_mul_f32 v[192:193], v[192:193], v[188:189] op_sel_hi:[1,0]
	v_lshlrev_b64 v[182:183], 12, v[182:183]
	v_cvt_pk_bf16_f32 v189, v192, v193
	v_cvt_pk_bf16_f32 v190, v190, v191
	v_cmp_gt_i32_e32 vcc, s86, v185
	v_cndmask_b32_e64 v1, v186, v189, s[8:9]
	v_cndmask_b32_e64 v192, v187, v190, s[8:9]
	s_nop 1
	v_permlane16_swap_b32_e32 v186, v189
	v_permlane16_swap_b32_e32 v187, v190
	v_lshl_add_u64 v[182:183], s[60:61], 0, v[182:183]
	s_and_saveexec_b64 s[10:11], vcc
	s_cbranch_execz .LBB0_1291
	s_waitcnt lgkmcnt(1)
	v_mov_b32_e32 v194, v186
	s_waitcnt lgkmcnt(0)
	v_mov_b32_e32 v195, v187
	v_mov_b32_e32 v196, v189
	v_mov_b32_e32 v197, v190
	v_lshl_add_u64 v[186:187], v[168:169], 1, v[182:183]
	global_store_dwordx4 v[186:187], v[194:197], off
.LBB0_1291:
	s_or_b64 exec, exec, s[10:11]
	v_mov_b32_e32 v189, v188
	s_waitcnt lgkmcnt(1)
	v_pk_add_f32 v[190:191], v[94:95], v[154:155]
	v_pk_add_f32 v[186:187], v[96:97], v[156:157]
	v_pk_mul_f32 v[190:191], v[190:191], v[188:189]
	s_waitcnt lgkmcnt(0)
	v_mov_b32_e32 v192, v188
	v_mov_b32_e32 v193, v188
	v_cvt_pk_bf16_f32 v185, v190, v191
	v_pk_add_f32 v[190:191], v[88:89], v[152:153]
	v_pk_add_f32 v[194:195], v[86:87], v[150:151]
	v_pk_mul_f32 v[186:187], v[186:187], v[192:193]
	v_pk_mul_f32 v[190:191], v[190:191], v[192:193]
	v_pk_mul_f32 v[188:189], v[194:195], v[188:189]
	v_cvt_pk_bf16_f32 v186, v186, v187
	s_nop 0
	v_cvt_pk_bf16_f32 v187, v188, v189
	v_cvt_pk_bf16_f32 v188, v190, v191
	s_nop 0
	v_cndmask_b32_e64 v1, v185, v187, s[8:9]
	v_cndmask_b32_e64 v190, v186, v188, s[8:9]
	s_nop 1
	v_permlane16_swap_b32_e32 v185, v187
	v_permlane16_swap_b32_e32 v186, v188
	s_and_saveexec_b64 s[10:11], vcc
	s_cbranch_execz .LBB0_1293
	s_waitcnt lgkmcnt(1)
	v_mov_b32_e32 v192, v185
	s_waitcnt lgkmcnt(0)
	v_mov_b32_e32 v193, v186
	v_mov_b32_e32 v194, v187
	v_mov_b32_e32 v195, v188
	v_lshl_add_u64 v[182:183], v[168:169], 1, v[182:183]
	global_store_dwordx4 v[182:183], v[192:195], off offset:64
.LBB0_1293:
	s_or_b64 exec, exec, s[10:11]
	v_pk_add_f32 v[182:183], v[84:85], v[164:165]
	v_pk_add_f32 v[186:187], v[82:83], v[162:163]
	s_waitcnt lgkmcnt(1)
	v_pk_mul_f32 v[188:189], v[182:183], v[184:185] op_sel_hi:[1,0]
	v_pk_mul_f32 v[182:183], v[186:187], v[184:185] op_sel_hi:[1,0]
	v_pk_add_f32 v[186:187], v[76:77], v[160:161]
	v_cvt_pk_bf16_f32 v182, v182, v183
	v_cvt_pk_bf16_f32 v183, v188, v189
	v_pk_add_f32 v[188:189], v[74:75], v[158:159]
	v_pk_mul_f32 v[186:187], v[186:187], v[184:185] op_sel_hi:[1,0]
	v_pk_mul_f32 v[188:189], v[188:189], v[184:185] op_sel_hi:[1,0]
	v_lshlrev_b64 v[180:181], 12, v[180:181]
	v_cvt_pk_bf16_f32 v185, v188, v189
	v_cvt_pk_bf16_f32 v186, v186, v187
	v_cmp_gt_i32_e32 vcc, s86, v179
	v_cndmask_b32_e64 v1, v182, v185, s[8:9]
	v_cndmask_b32_e64 v188, v183, v186, s[8:9]
	s_nop 1
	v_permlane16_swap_b32_e32 v182, v185
	v_permlane16_swap_b32_e32 v183, v186
	v_lshl_add_u64 v[180:181], s[60:61], 0, v[180:181]
	s_and_saveexec_b64 s[10:11], vcc
	s_cbranch_execz .LBB0_1295
	s_waitcnt lgkmcnt(1)
	v_mov_b32_e32 v190, v182
	s_waitcnt lgkmcnt(0)
	v_mov_b32_e32 v191, v183
	v_mov_b32_e32 v192, v185
	v_mov_b32_e32 v193, v186
	v_lshl_add_u64 v[182:183], v[168:169], 1, v[180:181]
	global_store_dwordx4 v[182:183], v[190:193], off
.LBB0_1295:
	s_or_b64 exec, exec, s[10:11]
	v_mov_b32_e32 v185, v184
	s_waitcnt lgkmcnt(1)
	v_pk_add_f32 v[186:187], v[78:79], v[154:155]
	v_pk_add_f32 v[182:183], v[80:81], v[156:157]
	v_pk_mul_f32 v[186:187], v[186:187], v[184:185]
	s_waitcnt lgkmcnt(0)
	v_mov_b32_e32 v188, v184
	v_mov_b32_e32 v189, v184
	v_cvt_pk_bf16_f32 v179, v186, v187
	v_pk_add_f32 v[186:187], v[72:73], v[152:153]
	v_pk_add_f32 v[190:191], v[70:71], v[150:151]
	v_pk_mul_f32 v[182:183], v[182:183], v[188:189]
	v_pk_mul_f32 v[186:187], v[186:187], v[188:189]
	v_pk_mul_f32 v[184:185], v[190:191], v[184:185]
	v_cvt_pk_bf16_f32 v182, v182, v183
	s_nop 0
	v_cvt_pk_bf16_f32 v183, v184, v185
	v_cvt_pk_bf16_f32 v184, v186, v187
	s_nop 0
	v_cndmask_b32_e64 v1, v179, v183, s[8:9]
	v_cndmask_b32_e64 v186, v182, v184, s[8:9]
	s_nop 1
	v_permlane16_swap_b32_e32 v179, v183
	v_permlane16_swap_b32_e32 v182, v184
	s_and_saveexec_b64 s[10:11], vcc
	s_cbranch_execz .LBB0_1297
	s_waitcnt lgkmcnt(1)
	v_mov_b32_e32 v188, v179
	s_waitcnt lgkmcnt(0)
	v_mov_b32_e32 v189, v182
	v_mov_b32_e32 v190, v183
	v_mov_b32_e32 v191, v184
	v_lshl_add_u64 v[180:181], v[168:169], 1, v[180:181]
	global_store_dwordx4 v[180:181], v[188:191], off offset:64
.LBB0_1297:
	s_or_b64 exec, exec, s[10:11]
	v_pk_add_f32 v[182:183], v[66:67], v[162:163]
	v_pk_add_f32 v[180:181], v[68:69], v[164:165]
	v_pk_mul_f32 v[182:183], v[182:183], v[178:179] op_sel_hi:[1,0]
	v_pk_mul_f32 v[180:181], v[180:181], v[178:179] op_sel_hi:[1,0]
	v_cvt_pk_bf16_f32 v179, v182, v183
	v_pk_add_f32 v[182:183], v[60:61], v[160:161]
	s_waitcnt lgkmcnt(1)
	v_pk_add_f32 v[184:185], v[58:59], v[158:159]
	v_pk_mul_f32 v[182:183], v[182:183], v[178:179] op_sel_hi:[1,0]
	v_pk_mul_f32 v[184:185], v[184:185], v[178:179] op_sel_hi:[1,0]
	v_cvt_pk_bf16_f32 v180, v180, v181
	v_lshlrev_b64 v[176:177], 12, v[176:177]
	v_cvt_pk_bf16_f32 v181, v184, v185
	v_cvt_pk_bf16_f32 v182, v182, v183
	v_cmp_gt_i32_e32 vcc, s86, v175
	v_cndmask_b32_e64 v1, v179, v181, s[8:9]
	v_cndmask_b32_e64 v184, v180, v182, s[8:9]
	s_nop 1
	v_permlane16_swap_b32_e32 v179, v181
	v_permlane16_swap_b32_e32 v180, v182
	v_lshl_add_u64 v[176:177], s[60:61], 0, v[176:177]
	s_and_saveexec_b64 s[10:11], vcc
	s_cbranch_execz .LBB0_1299
	s_waitcnt lgkmcnt(1)
	v_mov_b32_e32 v186, v179
	s_waitcnt lgkmcnt(0)
	v_mov_b32_e32 v187, v180
	v_mov_b32_e32 v188, v181
	v_mov_b32_e32 v189, v182
	v_lshl_add_u64 v[180:181], v[168:169], 1, v[176:177]
	global_store_dwordx4 v[180:181], v[186:189], off
.LBB0_1299:
	s_or_b64 exec, exec, s[10:11]
	v_mov_b32_e32 v179, v178
	s_waitcnt lgkmcnt(1)
	v_pk_add_f32 v[182:183], v[62:63], v[154:155]
	v_pk_add_f32 v[180:181], v[64:65], v[156:157]
	v_pk_mul_f32 v[182:183], v[182:183], v[178:179]
	s_waitcnt lgkmcnt(0)
	v_mov_b32_e32 v184, v178
	v_mov_b32_e32 v185, v178
	v_cvt_pk_bf16_f32 v175, v182, v183
	v_pk_add_f32 v[182:183], v[56:57], v[152:153]
	v_pk_add_f32 v[186:187], v[54:55], v[150:151]
	v_pk_mul_f32 v[180:181], v[180:181], v[184:185]
	v_pk_mul_f32 v[182:183], v[182:183], v[184:185]
	v_pk_mul_f32 v[178:179], v[186:187], v[178:179]
	v_cvt_pk_bf16_f32 v180, v180, v181
	s_nop 0
	v_cvt_pk_bf16_f32 v178, v178, v179
	v_cvt_pk_bf16_f32 v179, v182, v183
	s_nop 0
	v_cndmask_b32_e64 v1, v175, v178, s[8:9]
	v_cndmask_b32_e64 v182, v180, v179, s[8:9]
	s_nop 1
	v_permlane16_swap_b32_e32 v175, v178
	v_permlane16_swap_b32_e32 v180, v179
	s_and_saveexec_b64 s[10:11], vcc
	s_cbranch_execz .LBB0_1301
	s_waitcnt lgkmcnt(1)
	v_mov_b32_e32 v184, v175
	s_waitcnt lgkmcnt(0)
	v_mov_b32_e32 v185, v180
	v_mov_b32_e32 v186, v178
	v_mov_b32_e32 v187, v179
	v_lshl_add_u64 v[176:177], v[168:169], 1, v[176:177]
	global_store_dwordx4 v[176:177], v[184:187], off offset:64
.LBB0_1301:
	s_or_b64 exec, exec, s[10:11]
	v_pk_add_f32 v[178:179], v[50:51], v[162:163]
	v_pk_add_f32 v[176:177], v[52:53], v[164:165]
	s_waitcnt vmcnt(1)
	v_pk_mul_f32 v[178:179], v[178:179], v[174:175] op_sel_hi:[1,0]
	v_pk_mul_f32 v[176:177], v[176:177], v[174:175] op_sel_hi:[1,0]
	v_cvt_pk_bf16_f32 v175, v178, v179
	v_pk_add_f32 v[178:179], v[44:45], v[160:161]
	s_waitcnt lgkmcnt(1)
	v_pk_add_f32 v[180:181], v[42:43], v[158:159]
	v_pk_mul_f32 v[178:179], v[178:179], v[174:175] op_sel_hi:[1,0]
	v_pk_mul_f32 v[180:181], v[180:181], v[174:175] op_sel_hi:[1,0]
	v_cvt_pk_bf16_f32 v176, v176, v177
	v_lshlrev_b64 v[172:173], 12, v[172:173]
	v_cvt_pk_bf16_f32 v177, v180, v181
	v_cvt_pk_bf16_f32 v178, v178, v179
	v_cmp_gt_i32_e32 vcc, s86, v171
	v_cndmask_b32_e64 v1, v175, v177, s[8:9]
	v_cndmask_b32_e64 v180, v176, v178, s[8:9]
	s_nop 1
	v_permlane16_swap_b32_e32 v175, v177
	v_permlane16_swap_b32_e32 v176, v178
	v_lshl_add_u64 v[172:173], s[60:61], 0, v[172:173]
	s_and_saveexec_b64 s[10:11], vcc
	s_cbranch_execz .LBB0_1303
	s_waitcnt lgkmcnt(1)
	v_mov_b32_e32 v182, v175
	s_waitcnt lgkmcnt(0)
	v_mov_b32_e32 v183, v176
	v_mov_b32_e32 v184, v177
	v_mov_b32_e32 v185, v178
	v_lshl_add_u64 v[176:177], v[168:169], 1, v[172:173]
	global_store_dwordx4 v[176:177], v[182:185], off
.LBB0_1303:
	s_or_b64 exec, exec, s[10:11]
	v_mov_b32_e32 v175, v174
	s_waitcnt lgkmcnt(1)
	v_pk_add_f32 v[178:179], v[46:47], v[154:155]
	v_pk_add_f32 v[176:177], v[48:49], v[156:157]
	v_pk_mul_f32 v[178:179], v[178:179], v[174:175]
	s_waitcnt lgkmcnt(0)
	v_mov_b32_e32 v180, v174
	v_mov_b32_e32 v181, v174
	v_cvt_pk_bf16_f32 v171, v178, v179
	v_pk_add_f32 v[178:179], v[40:41], v[152:153]
	v_pk_add_f32 v[182:183], v[38:39], v[150:151]
	v_pk_mul_f32 v[176:177], v[176:177], v[180:181]
	v_pk_mul_f32 v[178:179], v[178:179], v[180:181]
	v_pk_mul_f32 v[174:175], v[182:183], v[174:175]
	v_cvt_pk_bf16_f32 v176, v176, v177
	s_nop 0
	v_cvt_pk_bf16_f32 v174, v174, v175
	v_cvt_pk_bf16_f32 v175, v178, v179
	s_nop 0
	v_cndmask_b32_e64 v1, v171, v174, s[8:9]
	v_cndmask_b32_e64 v178, v176, v175, s[8:9]
	s_nop 1
	v_permlane16_swap_b32_e32 v171, v174
	v_permlane16_swap_b32_e32 v176, v175
	s_and_saveexec_b64 s[10:11], vcc
	s_cbranch_execz .LBB0_1305
	s_waitcnt lgkmcnt(1)
	v_mov_b32_e32 v180, v171
	s_waitcnt lgkmcnt(0)
	v_mov_b32_e32 v181, v176
	v_mov_b32_e32 v182, v174
	v_mov_b32_e32 v183, v175
	v_lshl_add_u64 v[172:173], v[168:169], 1, v[172:173]
	global_store_dwordx4 v[172:173], v[180:183], off offset:64
.LBB0_1305:
	s_or_b64 exec, exec, s[10:11]
	v_pk_add_f32 v[164:165], v[36:37], v[164:165]
	v_pk_add_f32 v[162:163], v[34:35], v[162:163]
	v_pk_add_f32 v[158:159], v[26:27], v[158:159]
	s_waitcnt vmcnt(0)
	v_pk_mul_f32 v[164:165], v[164:165], v[170:171] op_sel_hi:[1,0]
	v_pk_mul_f32 v[162:163], v[162:163], v[170:171] op_sel_hi:[1,0]
	v_pk_add_f32 v[160:161], v[28:29], v[160:161]
	v_pk_mul_f32 v[158:159], v[158:159], v[170:171] op_sel_hi:[1,0]
	v_cvt_pk_bf16_f32 v162, v162, v163
	v_cvt_pk_bf16_f32 v163, v164, v165
	v_pk_mul_f32 v[164:165], v[160:161], v[170:171] op_sel_hi:[1,0]
	v_cvt_pk_bf16_f32 v160, v158, v159
	v_cmp_gt_i32_e32 vcc, s86, v5
	v_cvt_pk_bf16_f32 v161, v164, v165
	v_cndmask_b32_e64 v1, v162, v160, s[8:9]
	v_cndmask_b32_e64 v158, v163, v161, s[8:9]
	s_nop 1
	v_permlane16_swap_b32_e32 v162, v160
	v_permlane16_swap_b32_e32 v163, v161
	v_lshlrev_b64 v[158:159], 12, v[166:167]
	v_lshl_add_u64 v[158:159], s[60:61], 0, v[158:159]
	s_and_saveexec_b64 s[10:11], vcc
	s_cbranch_execz .LBB0_1307
	s_waitcnt lgkmcnt(1)
	s_waitcnt lgkmcnt(0)
	v_mov_b32_e32 v164, v160
	v_mov_b32_e32 v165, v161
	v_lshl_add_u64 v[160:161], v[168:169], 1, v[158:159]
	global_store_dwordx4 v[160:161], v[162:165], off
.LBB0_1307:
	s_or_b64 exec, exec, s[10:11]
	v_mov_b32_e32 v171, v170
	v_pk_add_f32 v[154:155], v[30:31], v[154:155]
	v_mov_b32_e32 v160, v170
	v_mov_b32_e32 v161, v170
	v_pk_add_f32 v[152:153], v[24:25], v[152:153]
	v_pk_add_f32 v[150:151], v[22:23], v[150:151]
	v_pk_add_f32 v[156:157], v[32:33], v[156:157]
	v_pk_mul_f32 v[154:155], v[154:155], v[170:171]
	v_pk_mul_f32 v[152:153], v[152:153], v[160:161]
	v_pk_mul_f32 v[150:151], v[150:151], v[170:171]
	v_pk_mul_f32 v[156:157], v[156:157], v[160:161]
	v_cvt_pk_bf16_f32 v5, v154, v155
	s_nop 0
	v_cvt_pk_bf16_f32 v154, v156, v157
	v_cvt_pk_bf16_f32 v150, v150, v151
	v_cvt_pk_bf16_f32 v151, v152, v153
	s_nop 0
	v_cndmask_b32_e64 v1, v5, v150, s[8:9]
	v_cndmask_b32_e64 v153, v154, v151, s[8:9]
	s_nop 1
	v_permlane16_swap_b32_e32 v5, v150
	v_permlane16_swap_b32_e32 v154, v151
	s_and_saveexec_b64 s[10:11], vcc
	s_cbranch_execz .LBB0_1309
	s_waitcnt lgkmcnt(1)
	v_mov_b32_e32 v160, v5
	s_waitcnt lgkmcnt(0)
	v_mov_b32_e32 v161, v154
	v_mov_b32_e32 v162, v150
	v_mov_b32_e32 v163, v151
	v_lshl_add_u64 v[150:151], v[168:169], 1, v[158:159]
	global_store_dwordx4 v[150:151], v[160:163], off offset:64

.LBB0_1310:
	s_lshl_b32 s2, s34, 5
	s_lshl_b32 s8, s48, 11
	s_add_i32 s2, s2, s46
	s_ashr_i32 s9, s8, 31
	v_add_u32_e32 v150, s2, v4
	s_lshl_b64 s[8:9], s[8:9], 2
	s_add_u32 s10, s12, s8
	v_ashrrev_i32_e32 v151, 31, v150
	s_addc_u32 s11, s13, s9
	v_lshlrev_b64 v[150:151], 2, v[150:151]
	s_waitcnt lgkmcnt(0)
	v_lshl_add_u64 v[152:153], s[10:11], 0, v[150:151]
	global_load_dwordx4 v[162:165], v[152:153], off
	global_load_dwordx4 v[154:157], v[152:153], off offset:64
	s_add_u32 s8, s16, s8
	s_addc_u32 s9, s17, s9
	v_lshl_add_u64 v[150:151], s[8:9], 0, v[150:151]
	global_load_dwordx4 v[158:161], v[150:151], off
	s_nop 0
	global_load_dwordx4 v[150:153], v[150:151], off offset:64
	v_cmp_eq_u32_e32 vcc, 0, v207
	s_add_i32 s5, s5, s4
	s_waitcnt vmcnt(3)
	v_add_f32_e32 v5, v147, v163
	v_cndmask_b32_e32 v1, v208, v4, vcc
	v_add_f32_e32 v4, v146, v162
	v_add_f32_e32 v146, v148, v164
	s_waitcnt vmcnt(2)
	v_add_f32_e32 v142, v142, v154
	v_min_f32_e32 v5, 0x40e00000, v5
	v_add_f32_e32 v147, v149, v165
	v_min_f32_e32 v4, 0x40e00000, v4
	v_min_f32_e32 v146, 0x40e00000, v146
	v_min_f32_e32 v142, 0x40e00000, v142
	v_mul_f32_e32 v149, 0xc01d265f, v5
	v_mul_f32_e32 v148, 0xc01d265f, v4
	v_mul_f32_e32 v166, 0xc01d265f, v146
	v_mul_f32_e32 v168, 0xc01d265f, v142
	v_exp_f32_e32 v149, v149
	v_exp_f32_e32 v148, v148
	v_exp_f32_e32 v166, v166
	v_exp_f32_e32 v168, v168
	v_add_f32_e32 v143, v143, v155
	v_add_f32_e32 v144, v144, v156
	v_add_f32_e32 v145, v145, v157
	v_min_f32_e32 v147, 0x40e00000, v147
	v_min_f32_e32 v143, 0x40e00000, v143
	v_min_f32_e32 v144, 0x40e00000, v144
	v_add_f32_e32 v149, 1.0, v149
	v_min_f32_e32 v145, 0x40e00000, v145
	v_mul_f32_e32 v167, 0xc01d265f, v147
	v_mul_f32_e32 v169, 0xc01d265f, v143
	v_mul_f32_e32 v170, 0xc01d265f, v144
	v_add_f32_e32 v148, 1.0, v148
	v_add_f32_e32 v166, 1.0, v166
	v_add_f32_e32 v168, 1.0, v168
	v_rcp_f32_e32 v149, v149
	v_mul_f32_e32 v171, 0xc01d265f, v145
	v_exp_f32_e32 v167, v167
	v_exp_f32_e32 v169, v169
	v_exp_f32_e32 v170, v170
	v_rcp_f32_e32 v148, v148
	v_rcp_f32_e32 v166, v166
	v_rcp_f32_e32 v168, v168
	s_waitcnt vmcnt(1)
	v_add_f32_e32 v139, v139, v159
	v_exp_f32_e32 v171, v171
	v_add_f32_e32 v138, v138, v158
	v_add_f32_e32 v140, v140, v160
	s_waitcnt vmcnt(0)
	v_add_f32_e32 v134, v134, v150
	v_med3_f32 v139, v139, s93, v212
	v_med3_f32 v138, v138, s93, v212
	v_med3_f32 v140, v140, s93, v212
	v_med3_f32 v134, v134, s93, v212
	v_add_f32_e32 v139, 1.0, v139
	v_mul_f32_e32 v5, v5, v149
	v_add_f32_e32 v138, 1.0, v138
	v_add_f32_e32 v140, 1.0, v140
	v_add_f32_e32 v134, 1.0, v134
	v_add_f32_e32 v167, 1.0, v167
	v_add_f32_e32 v169, 1.0, v169
	v_add_f32_e32 v170, 1.0, v170
	v_mul_f32_e32 v4, v4, v148
	v_mul_f32_e32 v146, v146, v166
	v_mul_f32_e32 v142, v142, v168
	v_mul_f32_e32 v5, v139, v5
	v_rcp_f32_e32 v167, v167
	v_rcp_f32_e32 v169, v169
	v_rcp_f32_e32 v170, v170
	v_mul_f32_e32 v4, v138, v4
	v_mul_f32_e32 v138, v140, v146
	v_mul_f32_e32 v140, v134, v142
	v_cvt_pk_bf16_f32 v134, v4, v5
	v_add_f32_e32 v5, 1.0, v171
	v_add_f32_e32 v136, v136, v152
	v_rcp_f32_e32 v5, v5
	v_add_f32_e32 v141, v141, v161
	v_add_f32_e32 v135, v135, v151
	v_med3_f32 v136, v136, s93, v212
	v_med3_f32 v141, v141, s93, v212
	v_med3_f32 v135, v135, s93, v212
	v_add_f32_e32 v4, 1.0, v136
	v_add_f32_e32 v136, v137, v153
	v_add_f32_e32 v141, 1.0, v141
	v_add_f32_e32 v135, 1.0, v135
	v_mul_f32_e32 v147, v147, v167
	v_mul_f32_e32 v143, v143, v169
	v_mul_f32_e32 v144, v144, v170
	v_med3_f32 v136, v136, s93, v212
	v_mul_f32_e32 v139, v141, v147
	v_mul_f32_e32 v141, v135, v143
	v_cvt_pk_bf16_f32 v135, v138, v139
	v_mul_f32_e32 v4, v4, v144
	v_mul_f32_e32 v5, v145, v5
	v_add_f32_e32 v136, 1.0, v136
	v_and_b32_e32 v138, 64, v206
	v_mul_f32_e32 v5, v136, v5
	v_cvt_pk_bf16_f32 v136, v140, v141
	v_cvt_pk_bf16_f32 v137, v4, v5
	v_xor_b32_e32 v4, 16, v206
	v_add_u32_e32 v138, 64, v138
	v_cmp_lt_i32_e64 s[8:9], v4, v138
	v_cndmask_b32_e32 v5, v134, v136, vcc
	v_cndmask_b32_e32 v139, v135, v137, vcc
	v_cndmask_b32_e64 v4, v206, v4, s[8:9]
	v_lshlrev_b32_e32 v4, 2, v4
	s_nop 1
	v_permlane16_swap_b32_e32 v134, v136
	v_permlane16_swap_b32_e32 v135, v137
	v_and_or_b32 v5, v3, 15, s5
	v_add_lshl_u32 v3, s2, v1, 1
	v_cmp_gt_i32_e64 s[8:9], s86, v5
	s_and_saveexec_b64 s[10:11], s[8:9]
	s_cbranch_execz .LBB0_1312
	v_add_u32_e32 v1, s85, v5
	s_waitcnt lgkmcnt(1)
	s_waitcnt lgkmcnt(0)
	v_lshl_add_u32 v1, v1, 12, v3
	buffer_store_dwordx4 v[134:137], v1, s[36:39], 0 offen sc1
.LBB0_1312:
	s_or_b64 exec, exec, s[10:11]
	v_add_f32_e32 v1, v130, v162
	v_min_f32_e32 v1, 0x40e00000, v1
	v_mul_f32_e32 v130, 0xc01d265f, v1
	v_exp_f32_e32 v130, v130
	v_add_f32_e32 v131, v131, v163
	v_min_f32_e32 v131, 0x40e00000, v131
	v_mul_f32_e32 v134, 0xc01d265f, v131
	v_add_f32_e32 v130, 1.0, v130
	v_rcp_f32_e32 v130, v130
	v_exp_f32_e32 v134, v134
	v_add_f32_e32 v126, v126, v158
	v_med3_f32 v126, v126, s93, v212
	v_mul_f32_e32 v1, v1, v130
	v_add_f32_e32 v130, 1.0, v134
	v_rcp_f32_e32 v130, v130
	v_add_f32_e32 v126, 1.0, v126
	v_mul_f32_e32 v1, v126, v1
	v_add_f32_e32 v126, v127, v159
	v_mul_f32_e32 v127, v131, v130
	v_add_f32_e32 v130, v132, v164
	v_min_f32_e32 v130, 0x40e00000, v130
	v_mul_f32_e32 v131, 0xc01d265f, v130
	v_exp_f32_e32 v131, v131
	v_med3_f32 v126, v126, s93, v212
	v_add_f32_e32 v126, 1.0, v126
	v_mul_f32_e32 v126, v126, v127
	v_add_f32_e32 v127, v128, v160
	v_add_f32_e32 v128, 1.0, v131
	v_add_f32_e32 v131, v133, v165
	v_min_f32_e32 v131, 0x40e00000, v131
	v_mul_f32_e32 v132, 0xc01d265f, v131
	v_rcp_f32_e32 v128, v128
	v_exp_f32_e32 v132, v132
	v_med3_f32 v127, v127, s93, v212
	v_add_f32_e32 v127, 1.0, v127
	v_mul_f32_e32 v128, v130, v128
	v_add_f32_e32 v130, 1.0, v132
	v_rcp_f32_e32 v130, v130
	v_mul_f32_e32 v127, v127, v128
	v_add_f32_e32 v128, v129, v161
	v_med3_f32 v128, v128, s93, v212
	v_mul_f32_e32 v129, v131, v130
	v_add_f32_e32 v128, 1.0, v128
	v_add_f32_e32 v122, v122, v154
	v_mul_f32_e32 v128, v128, v129
	v_min_f32_e32 v129, 0x40e00000, v122
	v_add_f32_e32 v123, v123, v155
	v_mul_f32_e32 v122, 0xc01d265f, v129
	v_min_f32_e32 v123, 0x40e00000, v123
	v_exp_f32_e32 v130, v122
	v_cvt_pk_bf16_f32 v122, v1, v126
	v_cvt_pk_bf16_f32 v126, v127, v128
	v_mul_f32_e32 v127, 0xc01d265f, v123
	v_exp_f32_e32 v127, v127
	v_add_f32_e32 v1, v118, v150
	v_add_f32_e32 v118, 1.0, v130
	v_rcp_f32_e32 v118, v118
	v_add_f32_e32 v127, 1.0, v127
	v_rcp_f32_e32 v127, v127
	v_med3_f32 v1, v1, s93, v212
	v_mul_f32_e32 v118, v129, v118
	v_add_f32_e32 v1, 1.0, v1
	v_mul_f32_e32 v1, v1, v118
	v_add_f32_e32 v118, v119, v151
	v_mul_f32_e32 v119, v123, v127
	v_add_f32_e32 v123, v124, v156
	v_min_f32_e32 v123, 0x40e00000, v123
	v_mul_f32_e32 v124, 0xc01d265f, v123
	v_exp_f32_e32 v124, v124
	v_med3_f32 v118, v118, s93, v212
	v_add_f32_e32 v118, 1.0, v118
	v_mul_f32_e32 v118, v118, v119
	v_add_f32_e32 v119, v120, v152
	v_add_f32_e32 v120, 1.0, v124
	v_add_f32_e32 v124, v125, v157
	v_min_f32_e32 v124, 0x40e00000, v124
	v_mul_f32_e32 v125, 0xc01d265f, v124
	v_rcp_f32_e32 v120, v120
	v_exp_f32_e32 v125, v125
	v_med3_f32 v119, v119, s93, v212
	v_add_f32_e32 v119, 1.0, v119
	v_mul_f32_e32 v120, v123, v120
	v_add_f32_e32 v123, 1.0, v125
	v_rcp_f32_e32 v123, v123
	v_mul_f32_e32 v119, v119, v120
	v_add_f32_e32 v120, v121, v153
	v_med3_f32 v120, v120, s93, v212
	v_mul_f32_e32 v121, v124, v123
	v_add_f32_e32 v120, 1.0, v120
	v_mul_f32_e32 v120, v120, v121
	v_cvt_pk_bf16_f32 v118, v1, v118
	v_cvt_pk_bf16_f32 v119, v119, v120
	s_nop 0
	v_cndmask_b32_e32 v1, v122, v118, vcc
	v_cndmask_b32_e32 v120, v126, v119, vcc
	s_nop 1
	v_permlane16_swap_b32_e32 v122, v118
	v_permlane16_swap_b32_e32 v126, v119
	v_or_b32_e32 v120, 16, v5
	v_cmp_gt_i32_e64 s[8:9], s86, v120
	s_and_saveexec_b64 s[10:11], s[8:9]
	s_cbranch_execz .LBB0_1314
	v_add_u32_e32 v1, s85, v120
	s_waitcnt lgkmcnt(1)
	v_mov_b32_e32 v124, v122
	s_waitcnt lgkmcnt(0)
	v_mov_b32_e32 v125, v126
	v_mov_b32_e32 v126, v118
	v_mov_b32_e32 v127, v119
	v_lshl_add_u32 v1, v1, 12, v3
	buffer_store_dwordx4 v[124:127], v1, s[36:39], 0 offen sc1
.LBB0_1314:
	s_or_b64 exec, exec, s[10:11]
	v_add_f32_e32 v1, v114, v162
	v_min_f32_e32 v1, 0x40e00000, v1
	v_mul_f32_e32 v114, 0xc01d265f, v1
	v_exp_f32_e32 v114, v114
	v_add_f32_e32 v115, v115, v163
	v_min_f32_e32 v115, 0x40e00000, v115
	v_mul_f32_e32 v118, 0xc01d265f, v115
	v_add_f32_e32 v114, 1.0, v114
	v_rcp_f32_e32 v114, v114
	v_exp_f32_e32 v118, v118
	v_add_f32_e32 v110, v110, v158
	v_med3_f32 v110, v110, s93, v212
	v_mul_f32_e32 v1, v1, v114
	v_add_f32_e32 v114, 1.0, v118
	v_rcp_f32_e32 v114, v114
	v_add_f32_e32 v110, 1.0, v110
	v_mul_f32_e32 v1, v110, v1
	v_add_f32_e32 v110, v111, v159
	v_mul_f32_e32 v111, v115, v114
	v_add_f32_e32 v114, v116, v164
	v_min_f32_e32 v114, 0x40e00000, v114
	v_mul_f32_e32 v115, 0xc01d265f, v114
	v_exp_f32_e32 v115, v115
	v_med3_f32 v110, v110, s93, v212
	v_add_f32_e32 v110, 1.0, v110
	v_mul_f32_e32 v110, v110, v111
	v_add_f32_e32 v111, v112, v160
	v_add_f32_e32 v112, 1.0, v115
	v_add_f32_e32 v115, v117, v165
	v_min_f32_e32 v115, 0x40e00000, v115
	v_mul_f32_e32 v116, 0xc01d265f, v115
	v_rcp_f32_e32 v112, v112
	v_exp_f32_e32 v116, v116
	v_med3_f32 v111, v111, s93, v212
	v_add_f32_e32 v111, 1.0, v111
	v_mul_f32_e32 v112, v114, v112
	v_add_f32_e32 v114, 1.0, v116
	v_rcp_f32_e32 v114, v114
	v_mul_f32_e32 v111, v111, v112
	v_add_f32_e32 v112, v113, v161
	v_med3_f32 v112, v112, s93, v212
	v_mul_f32_e32 v113, v115, v114
	v_add_f32_e32 v112, 1.0, v112
	v_add_f32_e32 v106, v106, v154
	v_mul_f32_e32 v112, v112, v113
	v_min_f32_e32 v113, 0x40e00000, v106
	v_add_f32_e32 v107, v107, v155
	v_mul_f32_e32 v106, 0xc01d265f, v113
	v_min_f32_e32 v107, 0x40e00000, v107
	v_exp_f32_e32 v114, v106
	v_cvt_pk_bf16_f32 v106, v1, v110
	v_cvt_pk_bf16_f32 v110, v111, v112
	v_mul_f32_e32 v111, 0xc01d265f, v107
	v_exp_f32_e32 v111, v111
	v_add_f32_e32 v1, v102, v150
	v_add_f32_e32 v102, 1.0, v114
	v_rcp_f32_e32 v102, v102
	v_add_f32_e32 v111, 1.0, v111
	v_rcp_f32_e32 v111, v111
	v_med3_f32 v1, v1, s93, v212
	v_mul_f32_e32 v102, v113, v102
	v_add_f32_e32 v1, 1.0, v1
	v_mul_f32_e32 v1, v1, v102
	v_add_f32_e32 v102, v103, v151
	v_mul_f32_e32 v103, v107, v111
	v_add_f32_e32 v107, v108, v156
	v_min_f32_e32 v107, 0x40e00000, v107
	v_mul_f32_e32 v108, 0xc01d265f, v107
	v_exp_f32_e32 v108, v108
	v_med3_f32 v102, v102, s93, v212
	v_add_f32_e32 v102, 1.0, v102
	v_mul_f32_e32 v102, v102, v103
	v_add_f32_e32 v103, v104, v152
	v_add_f32_e32 v104, 1.0, v108
	v_add_f32_e32 v108, v109, v157
	v_min_f32_e32 v108, 0x40e00000, v108
	v_mul_f32_e32 v109, 0xc01d265f, v108
	v_rcp_f32_e32 v104, v104
	v_exp_f32_e32 v109, v109
	v_med3_f32 v103, v103, s93, v212
	v_add_f32_e32 v103, 1.0, v103
	v_mul_f32_e32 v104, v107, v104
	v_add_f32_e32 v107, 1.0, v109
	v_rcp_f32_e32 v107, v107
	v_mul_f32_e32 v103, v103, v104
	v_add_f32_e32 v104, v105, v153
	v_med3_f32 v104, v104, s93, v212
	v_mul_f32_e32 v105, v108, v107
	v_add_f32_e32 v104, 1.0, v104
	v_mul_f32_e32 v104, v104, v105
	v_cvt_pk_bf16_f32 v102, v1, v102
	v_cvt_pk_bf16_f32 v103, v103, v104
	s_nop 0
	v_cndmask_b32_e32 v1, v106, v102, vcc
	v_cndmask_b32_e32 v104, v110, v103, vcc
	s_nop 1
	v_permlane16_swap_b32_e32 v106, v102
	v_permlane16_swap_b32_e32 v110, v103
	v_or_b32_e32 v104, 32, v5
	v_cmp_gt_i32_e64 s[8:9], s86, v104
	s_and_saveexec_b64 s[10:11], s[8:9]
	s_cbranch_execz .LBB0_1316
	v_add_u32_e32 v1, s85, v104
	s_waitcnt lgkmcnt(1)
	v_mov_b32_e32 v108, v106
	s_waitcnt lgkmcnt(0)
	v_mov_b32_e32 v109, v110
	v_mov_b32_e32 v110, v102
	v_mov_b32_e32 v111, v103
	v_lshl_add_u32 v1, v1, 12, v3
	buffer_store_dwordx4 v[108:111], v1, s[36:39], 0 offen sc1
.LBB0_1316:
	s_or_b64 exec, exec, s[10:11]
	v_add_f32_e32 v1, v98, v162
	v_min_f32_e32 v1, 0x40e00000, v1
	v_mul_f32_e32 v98, 0xc01d265f, v1
	v_exp_f32_e32 v98, v98
	v_add_f32_e32 v99, v99, v163
	v_min_f32_e32 v99, 0x40e00000, v99
	v_mul_f32_e32 v102, 0xc01d265f, v99
	v_add_f32_e32 v98, 1.0, v98
	v_rcp_f32_e32 v98, v98
	v_exp_f32_e32 v102, v102
	v_add_f32_e32 v94, v94, v158
	v_med3_f32 v94, v94, s93, v212
	v_mul_f32_e32 v1, v1, v98
	v_add_f32_e32 v98, 1.0, v102
	v_rcp_f32_e32 v98, v98
	v_add_f32_e32 v94, 1.0, v94
	v_mul_f32_e32 v1, v94, v1
	v_add_f32_e32 v94, v95, v159
	v_mul_f32_e32 v95, v99, v98
	v_add_f32_e32 v98, v100, v164
	v_min_f32_e32 v98, 0x40e00000, v98
	v_mul_f32_e32 v99, 0xc01d265f, v98
	v_exp_f32_e32 v99, v99
	v_med3_f32 v94, v94, s93, v212
	v_add_f32_e32 v94, 1.0, v94
	v_mul_f32_e32 v94, v94, v95
	v_add_f32_e32 v95, v96, v160
	v_add_f32_e32 v96, 1.0, v99
	v_add_f32_e32 v99, v101, v165
	v_min_f32_e32 v99, 0x40e00000, v99
	v_mul_f32_e32 v100, 0xc01d265f, v99
	v_rcp_f32_e32 v96, v96
	v_exp_f32_e32 v100, v100
	v_med3_f32 v95, v95, s93, v212
	v_add_f32_e32 v95, 1.0, v95
	v_mul_f32_e32 v96, v98, v96
	v_add_f32_e32 v98, 1.0, v100
	v_rcp_f32_e32 v98, v98
	v_mul_f32_e32 v95, v95, v96
	v_add_f32_e32 v96, v97, v161
	v_med3_f32 v96, v96, s93, v212
	v_mul_f32_e32 v97, v99, v98
	v_add_f32_e32 v96, 1.0, v96
	v_add_f32_e32 v90, v90, v154
	v_mul_f32_e32 v96, v96, v97
	v_min_f32_e32 v97, 0x40e00000, v90
	v_add_f32_e32 v91, v91, v155
	v_mul_f32_e32 v90, 0xc01d265f, v97
	v_min_f32_e32 v91, 0x40e00000, v91
	v_exp_f32_e32 v98, v90
	v_cvt_pk_bf16_f32 v90, v1, v94
	v_cvt_pk_bf16_f32 v94, v95, v96
	v_mul_f32_e32 v95, 0xc01d265f, v91
	v_exp_f32_e32 v95, v95
	v_add_f32_e32 v1, v86, v150
	v_add_f32_e32 v86, 1.0, v98
	v_rcp_f32_e32 v86, v86
	v_add_f32_e32 v95, 1.0, v95
	v_rcp_f32_e32 v95, v95
	v_med3_f32 v1, v1, s93, v212
	v_mul_f32_e32 v86, v97, v86
	v_add_f32_e32 v1, 1.0, v1
	v_mul_f32_e32 v1, v1, v86
	v_add_f32_e32 v86, v87, v151
	v_mul_f32_e32 v87, v91, v95
	v_add_f32_e32 v91, v92, v156
	v_min_f32_e32 v91, 0x40e00000, v91
	v_mul_f32_e32 v92, 0xc01d265f, v91
	v_exp_f32_e32 v92, v92
	v_med3_f32 v86, v86, s93, v212
	v_add_f32_e32 v86, 1.0, v86
	v_mul_f32_e32 v86, v86, v87
	v_add_f32_e32 v87, v88, v152
	v_add_f32_e32 v88, 1.0, v92
	v_add_f32_e32 v92, v93, v157
	v_min_f32_e32 v92, 0x40e00000, v92
	v_mul_f32_e32 v93, 0xc01d265f, v92
	v_rcp_f32_e32 v88, v88
	v_exp_f32_e32 v93, v93
	v_med3_f32 v87, v87, s93, v212
	v_add_f32_e32 v87, 1.0, v87
	v_mul_f32_e32 v88, v91, v88
	v_add_f32_e32 v91, 1.0, v93
	v_rcp_f32_e32 v91, v91
	v_mul_f32_e32 v87, v87, v88
	v_add_f32_e32 v88, v89, v153
	v_med3_f32 v88, v88, s93, v212
	v_mul_f32_e32 v89, v92, v91
	v_add_f32_e32 v88, 1.0, v88
	v_mul_f32_e32 v88, v88, v89
	v_cvt_pk_bf16_f32 v86, v1, v86
	v_cvt_pk_bf16_f32 v87, v87, v88
	s_nop 0
	v_cndmask_b32_e32 v1, v90, v86, vcc
	v_cndmask_b32_e32 v88, v94, v87, vcc
	s_nop 1
	v_permlane16_swap_b32_e32 v90, v86
	v_permlane16_swap_b32_e32 v94, v87
	v_or_b32_e32 v88, 48, v5
	v_cmp_gt_i32_e64 s[8:9], s86, v88
	s_and_saveexec_b64 s[10:11], s[8:9]
	s_cbranch_execz .LBB0_1318
	v_add_u32_e32 v1, s85, v88
	s_waitcnt lgkmcnt(1)
	v_mov_b32_e32 v92, v90
	s_waitcnt lgkmcnt(0)
	v_mov_b32_e32 v93, v94
	v_mov_b32_e32 v94, v86
	v_mov_b32_e32 v95, v87
	v_lshl_add_u32 v1, v1, 12, v3
	buffer_store_dwordx4 v[92:95], v1, s[36:39], 0 offen sc1
.LBB0_1318:
	s_or_b64 exec, exec, s[10:11]
	v_add_f32_e32 v1, v82, v162
	v_min_f32_e32 v1, 0x40e00000, v1
	v_mul_f32_e32 v82, 0xc01d265f, v1
	v_exp_f32_e32 v82, v82
	v_add_f32_e32 v83, v83, v163
	v_min_f32_e32 v83, 0x40e00000, v83
	v_mul_f32_e32 v86, 0xc01d265f, v83
	v_add_f32_e32 v82, 1.0, v82
	v_rcp_f32_e32 v82, v82
	v_exp_f32_e32 v86, v86
	v_add_f32_e32 v78, v78, v158
	v_med3_f32 v78, v78, s93, v212
	v_mul_f32_e32 v1, v1, v82
	v_add_f32_e32 v82, 1.0, v86
	v_rcp_f32_e32 v82, v82
	v_add_f32_e32 v78, 1.0, v78
	v_mul_f32_e32 v1, v78, v1
	v_add_f32_e32 v78, v79, v159
	v_mul_f32_e32 v79, v83, v82
	v_add_f32_e32 v82, v84, v164
	v_min_f32_e32 v82, 0x40e00000, v82
	v_mul_f32_e32 v83, 0xc01d265f, v82
	v_exp_f32_e32 v83, v83
	v_med3_f32 v78, v78, s93, v212
	v_add_f32_e32 v78, 1.0, v78
	v_mul_f32_e32 v78, v78, v79
	v_add_f32_e32 v79, v80, v160
	v_add_f32_e32 v80, 1.0, v83
	v_add_f32_e32 v83, v85, v165
	v_min_f32_e32 v83, 0x40e00000, v83
	v_mul_f32_e32 v84, 0xc01d265f, v83
	v_rcp_f32_e32 v80, v80
	v_exp_f32_e32 v84, v84
	v_med3_f32 v79, v79, s93, v212
	v_add_f32_e32 v79, 1.0, v79
	v_mul_f32_e32 v80, v82, v80
	v_add_f32_e32 v82, 1.0, v84
	v_rcp_f32_e32 v82, v82
	v_mul_f32_e32 v79, v79, v80
	v_add_f32_e32 v80, v81, v161
	v_med3_f32 v80, v80, s93, v212
	v_mul_f32_e32 v81, v83, v82
	v_add_f32_e32 v80, 1.0, v80
	v_add_f32_e32 v74, v74, v154
	v_mul_f32_e32 v80, v80, v81
	v_min_f32_e32 v81, 0x40e00000, v74
	v_add_f32_e32 v75, v75, v155
	v_mul_f32_e32 v74, 0xc01d265f, v81
	v_min_f32_e32 v75, 0x40e00000, v75
	v_exp_f32_e32 v82, v74
	v_cvt_pk_bf16_f32 v74, v1, v78
	v_cvt_pk_bf16_f32 v78, v79, v80
	v_mul_f32_e32 v79, 0xc01d265f, v75
	v_exp_f32_e32 v79, v79
	v_add_f32_e32 v1, v70, v150
	v_add_f32_e32 v70, 1.0, v82
	v_rcp_f32_e32 v70, v70
	v_add_f32_e32 v79, 1.0, v79
	v_rcp_f32_e32 v79, v79
	v_med3_f32 v1, v1, s93, v212
	v_mul_f32_e32 v70, v81, v70
	v_add_f32_e32 v1, 1.0, v1
	v_mul_f32_e32 v1, v1, v70
	v_add_f32_e32 v70, v71, v151
	v_mul_f32_e32 v71, v75, v79
	v_add_f32_e32 v75, v76, v156
	v_min_f32_e32 v75, 0x40e00000, v75
	v_mul_f32_e32 v76, 0xc01d265f, v75
	v_exp_f32_e32 v76, v76
	v_med3_f32 v70, v70, s93, v212
	v_add_f32_e32 v70, 1.0, v70
	v_mul_f32_e32 v70, v70, v71
	v_add_f32_e32 v71, v72, v152
	v_add_f32_e32 v72, 1.0, v76
	v_add_f32_e32 v76, v77, v157
	v_min_f32_e32 v76, 0x40e00000, v76
	v_mul_f32_e32 v77, 0xc01d265f, v76
	v_rcp_f32_e32 v72, v72
	v_exp_f32_e32 v77, v77
	v_med3_f32 v71, v71, s93, v212
	v_add_f32_e32 v71, 1.0, v71
	v_mul_f32_e32 v72, v75, v72
	v_add_f32_e32 v75, 1.0, v77
	v_rcp_f32_e32 v75, v75
	v_mul_f32_e32 v71, v71, v72
	v_add_f32_e32 v72, v73, v153
	v_med3_f32 v72, v72, s93, v212
	v_mul_f32_e32 v73, v76, v75
	v_add_f32_e32 v72, 1.0, v72
	v_mul_f32_e32 v72, v72, v73
	v_cvt_pk_bf16_f32 v70, v1, v70
	v_cvt_pk_bf16_f32 v71, v71, v72
	s_nop 0
	v_cndmask_b32_e32 v1, v74, v70, vcc
	v_cndmask_b32_e32 v72, v78, v71, vcc
	s_nop 1
	v_permlane16_swap_b32_e32 v74, v70
	v_permlane16_swap_b32_e32 v78, v71
	v_or_b32_e32 v72, 64, v5
	v_cmp_gt_i32_e64 s[8:9], s86, v72
	s_and_saveexec_b64 s[10:11], s[8:9]
	s_cbranch_execz .LBB0_1320
	v_add_u32_e32 v1, s85, v72
	s_waitcnt lgkmcnt(1)
	v_mov_b32_e32 v76, v74
	s_waitcnt lgkmcnt(0)
	v_mov_b32_e32 v77, v78
	v_mov_b32_e32 v78, v70
	v_mov_b32_e32 v79, v71
	v_lshl_add_u32 v1, v1, 12, v3
	buffer_store_dwordx4 v[76:79], v1, s[36:39], 0 offen sc1
.LBB0_1320:
	s_or_b64 exec, exec, s[10:11]
	v_add_f32_e32 v1, v66, v162
	v_min_f32_e32 v1, 0x40e00000, v1
	v_mul_f32_e32 v66, 0xc01d265f, v1
	v_exp_f32_e32 v66, v66
	v_add_f32_e32 v67, v67, v163
	v_min_f32_e32 v67, 0x40e00000, v67
	v_mul_f32_e32 v70, 0xc01d265f, v67
	v_add_f32_e32 v66, 1.0, v66
	v_rcp_f32_e32 v66, v66
	v_exp_f32_e32 v70, v70
	v_add_f32_e32 v62, v62, v158
	v_med3_f32 v62, v62, s93, v212
	v_mul_f32_e32 v1, v1, v66
	v_add_f32_e32 v66, 1.0, v70
	v_rcp_f32_e32 v66, v66
	v_add_f32_e32 v62, 1.0, v62
	v_mul_f32_e32 v1, v62, v1
	v_add_f32_e32 v62, v63, v159
	v_mul_f32_e32 v63, v67, v66
	v_add_f32_e32 v66, v68, v164
	v_min_f32_e32 v66, 0x40e00000, v66
	v_mul_f32_e32 v67, 0xc01d265f, v66
	v_exp_f32_e32 v67, v67
	v_med3_f32 v62, v62, s93, v212
	v_add_f32_e32 v62, 1.0, v62
	v_mul_f32_e32 v62, v62, v63
	v_add_f32_e32 v63, v64, v160
	v_add_f32_e32 v64, 1.0, v67
	v_add_f32_e32 v67, v69, v165
	v_min_f32_e32 v67, 0x40e00000, v67
	v_mul_f32_e32 v68, 0xc01d265f, v67
	v_rcp_f32_e32 v64, v64
	v_exp_f32_e32 v68, v68
	v_med3_f32 v63, v63, s93, v212
	v_add_f32_e32 v63, 1.0, v63
	v_mul_f32_e32 v64, v66, v64
	v_add_f32_e32 v66, 1.0, v68
	v_rcp_f32_e32 v66, v66
	v_mul_f32_e32 v63, v63, v64
	v_add_f32_e32 v64, v65, v161
	v_med3_f32 v64, v64, s93, v212
	v_mul_f32_e32 v65, v67, v66
	v_add_f32_e32 v64, 1.0, v64
	v_add_f32_e32 v58, v58, v154
	v_mul_f32_e32 v64, v64, v65
	v_min_f32_e32 v65, 0x40e00000, v58
	v_add_f32_e32 v59, v59, v155
	v_mul_f32_e32 v58, 0xc01d265f, v65
	v_min_f32_e32 v59, 0x40e00000, v59
	v_exp_f32_e32 v66, v58
	v_cvt_pk_bf16_f32 v58, v1, v62
	v_cvt_pk_bf16_f32 v62, v63, v64
	v_mul_f32_e32 v63, 0xc01d265f, v59
	v_exp_f32_e32 v63, v63
	v_add_f32_e32 v1, v54, v150
	v_add_f32_e32 v54, 1.0, v66
	v_rcp_f32_e32 v54, v54
	v_add_f32_e32 v63, 1.0, v63
	v_rcp_f32_e32 v63, v63
	v_med3_f32 v1, v1, s93, v212
	v_mul_f32_e32 v54, v65, v54
	v_add_f32_e32 v1, 1.0, v1
	v_mul_f32_e32 v1, v1, v54
	v_add_f32_e32 v54, v55, v151
	v_mul_f32_e32 v55, v59, v63
	v_add_f32_e32 v59, v60, v156
	v_min_f32_e32 v59, 0x40e00000, v59
	v_mul_f32_e32 v60, 0xc01d265f, v59
	v_exp_f32_e32 v60, v60
	v_med3_f32 v54, v54, s93, v212
	v_add_f32_e32 v54, 1.0, v54
	v_mul_f32_e32 v54, v54, v55
	v_add_f32_e32 v55, v56, v152
	v_add_f32_e32 v56, 1.0, v60
	v_add_f32_e32 v60, v61, v157
	v_min_f32_e32 v60, 0x40e00000, v60
	v_mul_f32_e32 v61, 0xc01d265f, v60
	v_rcp_f32_e32 v56, v56
	v_exp_f32_e32 v61, v61
	v_med3_f32 v55, v55, s93, v212
	v_add_f32_e32 v55, 1.0, v55
	v_mul_f32_e32 v56, v59, v56
	v_add_f32_e32 v59, 1.0, v61
	v_rcp_f32_e32 v59, v59
	v_mul_f32_e32 v55, v55, v56
	v_add_f32_e32 v56, v57, v153
	v_med3_f32 v56, v56, s93, v212
	v_mul_f32_e32 v57, v60, v59
	v_add_f32_e32 v56, 1.0, v56
	v_mul_f32_e32 v56, v56, v57
	v_cvt_pk_bf16_f32 v54, v1, v54
	v_cvt_pk_bf16_f32 v55, v55, v56
	s_nop 0
	v_cndmask_b32_e32 v1, v58, v54, vcc
	v_cndmask_b32_e32 v56, v62, v55, vcc
	s_nop 1
	v_permlane16_swap_b32_e32 v58, v54
	v_permlane16_swap_b32_e32 v62, v55
	v_or_b32_e32 v56, 0x50, v5
	v_cmp_gt_i32_e64 s[8:9], s86, v56
	s_and_saveexec_b64 s[10:11], s[8:9]
	s_cbranch_execz .LBB0_1322
	v_add_u32_e32 v1, s85, v56
	s_waitcnt lgkmcnt(1)
	v_mov_b32_e32 v60, v58
	s_waitcnt lgkmcnt(0)
	v_mov_b32_e32 v61, v62
	v_mov_b32_e32 v62, v54
	v_mov_b32_e32 v63, v55
	v_lshl_add_u32 v1, v1, 12, v3
	buffer_store_dwordx4 v[60:63], v1, s[36:39], 0 offen sc1
.LBB0_1322:
	s_or_b64 exec, exec, s[10:11]
	v_add_f32_e32 v1, v50, v162
	v_min_f32_e32 v1, 0x40e00000, v1
	v_mul_f32_e32 v50, 0xc01d265f, v1
	v_exp_f32_e32 v50, v50
	v_add_f32_e32 v51, v51, v163
	v_min_f32_e32 v51, 0x40e00000, v51
	v_mul_f32_e32 v54, 0xc01d265f, v51
	v_add_f32_e32 v50, 1.0, v50
	v_rcp_f32_e32 v50, v50
	v_exp_f32_e32 v54, v54
	v_add_f32_e32 v46, v46, v158
	v_med3_f32 v46, v46, s93, v212
	v_mul_f32_e32 v1, v1, v50
	v_add_f32_e32 v50, 1.0, v54
	v_rcp_f32_e32 v50, v50
	v_add_f32_e32 v46, 1.0, v46
	v_mul_f32_e32 v1, v46, v1
	v_add_f32_e32 v46, v47, v159
	v_mul_f32_e32 v47, v51, v50
	v_add_f32_e32 v50, v52, v164
	v_min_f32_e32 v50, 0x40e00000, v50
	v_mul_f32_e32 v51, 0xc01d265f, v50
	v_exp_f32_e32 v51, v51
	v_med3_f32 v46, v46, s93, v212
	v_add_f32_e32 v46, 1.0, v46
	v_mul_f32_e32 v46, v46, v47
	v_add_f32_e32 v47, v48, v160
	v_add_f32_e32 v48, 1.0, v51
	v_add_f32_e32 v51, v53, v165
	v_min_f32_e32 v51, 0x40e00000, v51
	v_mul_f32_e32 v52, 0xc01d265f, v51
	v_rcp_f32_e32 v48, v48
	v_exp_f32_e32 v52, v52
	v_med3_f32 v47, v47, s93, v212
	v_add_f32_e32 v47, 1.0, v47
	v_mul_f32_e32 v48, v50, v48
	v_add_f32_e32 v50, 1.0, v52
	v_rcp_f32_e32 v50, v50
	v_mul_f32_e32 v47, v47, v48
	v_add_f32_e32 v48, v49, v161
	v_med3_f32 v48, v48, s93, v212
	v_mul_f32_e32 v49, v51, v50
	v_add_f32_e32 v48, 1.0, v48
	v_add_f32_e32 v42, v42, v154
	v_mul_f32_e32 v48, v48, v49
	v_min_f32_e32 v49, 0x40e00000, v42
	v_add_f32_e32 v43, v43, v155
	v_mul_f32_e32 v42, 0xc01d265f, v49
	v_min_f32_e32 v43, 0x40e00000, v43
	v_exp_f32_e32 v50, v42
	v_cvt_pk_bf16_f32 v42, v1, v46
	v_cvt_pk_bf16_f32 v46, v47, v48
	v_mul_f32_e32 v47, 0xc01d265f, v43
	v_exp_f32_e32 v47, v47
	v_add_f32_e32 v1, v38, v150
	v_add_f32_e32 v38, 1.0, v50
	v_rcp_f32_e32 v38, v38
	v_add_f32_e32 v47, 1.0, v47
	v_rcp_f32_e32 v47, v47
	v_med3_f32 v1, v1, s93, v212
	v_mul_f32_e32 v38, v49, v38
	v_add_f32_e32 v1, 1.0, v1
	v_mul_f32_e32 v1, v1, v38
	v_add_f32_e32 v38, v39, v151
	v_mul_f32_e32 v39, v43, v47
	v_add_f32_e32 v43, v44, v156
	v_min_f32_e32 v43, 0x40e00000, v43
	v_mul_f32_e32 v44, 0xc01d265f, v43
	v_exp_f32_e32 v44, v44
	v_med3_f32 v38, v38, s93, v212
	v_add_f32_e32 v38, 1.0, v38
	v_mul_f32_e32 v38, v38, v39
	v_add_f32_e32 v39, v40, v152
	v_add_f32_e32 v40, 1.0, v44
	v_add_f32_e32 v44, v45, v157
	v_min_f32_e32 v44, 0x40e00000, v44
	v_mul_f32_e32 v45, 0xc01d265f, v44
	v_rcp_f32_e32 v40, v40
	v_exp_f32_e32 v45, v45
	v_med3_f32 v39, v39, s93, v212
	v_add_f32_e32 v39, 1.0, v39
	v_mul_f32_e32 v40, v43, v40
	v_add_f32_e32 v43, 1.0, v45
	v_rcp_f32_e32 v43, v43
	v_mul_f32_e32 v39, v39, v40
	v_add_f32_e32 v40, v41, v153
	v_med3_f32 v40, v40, s93, v212
	v_mul_f32_e32 v41, v44, v43
	v_add_f32_e32 v40, 1.0, v40
	v_mul_f32_e32 v40, v40, v41
	v_cvt_pk_bf16_f32 v38, v1, v38
	v_cvt_pk_bf16_f32 v39, v39, v40
	s_nop 0
	v_cndmask_b32_e32 v1, v42, v38, vcc
	v_cndmask_b32_e32 v40, v46, v39, vcc
	s_nop 1
	v_permlane16_swap_b32_e32 v42, v38
	v_permlane16_swap_b32_e32 v46, v39
	v_or_b32_e32 v40, 0x60, v5
	v_cmp_gt_i32_e64 s[8:9], s86, v40
	s_and_saveexec_b64 s[10:11], s[8:9]
	s_cbranch_execz .LBB0_1324
	v_add_u32_e32 v1, s85, v40
	s_waitcnt lgkmcnt(1)
	v_mov_b32_e32 v44, v42
	s_waitcnt lgkmcnt(0)
	v_mov_b32_e32 v45, v46
	v_mov_b32_e32 v46, v38
	v_mov_b32_e32 v47, v39
	v_lshl_add_u32 v1, v1, 12, v3
	buffer_store_dwordx4 v[44:47], v1, s[36:39], 0 offen sc1
.LBB0_1324:
	s_or_b64 exec, exec, s[10:11]
	v_add_f32_e32 v1, v34, v162
	v_min_f32_e32 v1, 0x40e00000, v1
	v_mul_f32_e32 v34, 0xc01d265f, v1
	v_exp_f32_e32 v34, v34
	v_add_f32_e32 v35, v35, v163
	v_min_f32_e32 v35, 0x40e00000, v35
	v_mul_f32_e32 v38, 0xc01d265f, v35
	v_add_f32_e32 v34, 1.0, v34
	v_rcp_f32_e32 v34, v34
	v_exp_f32_e32 v38, v38
	v_add_f32_e32 v30, v30, v158
	v_med3_f32 v30, v30, s93, v212
	v_mul_f32_e32 v1, v1, v34
	v_add_f32_e32 v34, 1.0, v38
	v_rcp_f32_e32 v34, v34
	v_add_f32_e32 v30, 1.0, v30
	v_mul_f32_e32 v1, v30, v1
	v_add_f32_e32 v30, v31, v159
	v_mul_f32_e32 v31, v35, v34
	v_add_f32_e32 v34, v36, v164
	v_min_f32_e32 v34, 0x40e00000, v34
	v_mul_f32_e32 v35, 0xc01d265f, v34
	v_exp_f32_e32 v35, v35
	v_med3_f32 v30, v30, s93, v212
	v_add_f32_e32 v30, 1.0, v30
	v_mul_f32_e32 v30, v30, v31
	v_add_f32_e32 v31, v32, v160
	v_add_f32_e32 v32, 1.0, v35
	v_add_f32_e32 v35, v37, v165
	v_min_f32_e32 v35, 0x40e00000, v35
	v_mul_f32_e32 v36, 0xc01d265f, v35
	v_rcp_f32_e32 v32, v32
	v_exp_f32_e32 v36, v36
	v_med3_f32 v31, v31, s93, v212
	v_add_f32_e32 v31, 1.0, v31
	v_mul_f32_e32 v32, v34, v32
	v_add_f32_e32 v34, 1.0, v36
	v_rcp_f32_e32 v34, v34
	v_mul_f32_e32 v31, v31, v32
	v_add_f32_e32 v32, v33, v161
	v_med3_f32 v32, v32, s93, v212
	v_mul_f32_e32 v33, v35, v34
	v_add_f32_e32 v32, 1.0, v32
	v_add_f32_e32 v26, v26, v154
	v_mul_f32_e32 v32, v32, v33
	v_min_f32_e32 v33, 0x40e00000, v26
	v_add_f32_e32 v27, v27, v155
	v_mul_f32_e32 v26, 0xc01d265f, v33
	v_min_f32_e32 v27, 0x40e00000, v27
	v_exp_f32_e32 v34, v26
	v_cvt_pk_bf16_f32 v26, v1, v30
	v_cvt_pk_bf16_f32 v30, v31, v32
	v_mul_f32_e32 v31, 0xc01d265f, v27
	v_exp_f32_e32 v31, v31
	v_add_f32_e32 v1, v22, v150
	v_add_f32_e32 v22, 1.0, v34
	v_rcp_f32_e32 v22, v22
	v_add_f32_e32 v31, 1.0, v31
	v_rcp_f32_e32 v31, v31
	v_med3_f32 v1, v1, s93, v212
	v_mul_f32_e32 v22, v33, v22
	v_add_f32_e32 v1, 1.0, v1
	v_mul_f32_e32 v1, v1, v22
	v_add_f32_e32 v22, v23, v151
	v_mul_f32_e32 v23, v27, v31
	v_add_f32_e32 v27, v28, v156
	v_min_f32_e32 v27, 0x40e00000, v27
	v_mul_f32_e32 v28, 0xc01d265f, v27
	v_exp_f32_e32 v28, v28
	v_med3_f32 v22, v22, s93, v212
	v_add_f32_e32 v22, 1.0, v22
	v_mul_f32_e32 v22, v22, v23
	v_add_f32_e32 v23, v24, v152
	v_add_f32_e32 v24, 1.0, v28
	v_add_f32_e32 v28, v29, v157
	v_min_f32_e32 v28, 0x40e00000, v28
	v_mul_f32_e32 v29, 0xc01d265f, v28
	v_rcp_f32_e32 v24, v24
	v_exp_f32_e32 v29, v29
	v_med3_f32 v23, v23, s93, v212
	v_add_f32_e32 v23, 1.0, v23
	v_mul_f32_e32 v24, v27, v24
	v_add_f32_e32 v27, 1.0, v29
	v_rcp_f32_e32 v27, v27
	v_mul_f32_e32 v23, v23, v24
	v_add_f32_e32 v24, v25, v153
	v_med3_f32 v24, v24, s93, v212
	v_mul_f32_e32 v25, v28, v27
	v_add_f32_e32 v24, 1.0, v24
	v_mul_f32_e32 v24, v24, v25
	v_cvt_pk_bf16_f32 v22, v1, v22
	v_cvt_pk_bf16_f32 v23, v23, v24
	s_nop 0
	v_cndmask_b32_e32 v1, v26, v22, vcc
	v_cndmask_b32_e32 v25, v30, v23, vcc
	s_nop 1
	v_permlane16_swap_b32_e32 v26, v22
	v_permlane16_swap_b32_e32 v30, v23
	v_or_b32_e32 v4, 0x70, v5
	v_cmp_gt_i32_e64 s[8:9], s86, v4
	s_and_saveexec_b64 s[10:11], s[8:9]
	s_cbranch_execz .LBB0_1326
	v_add_u32_e32 v1, s85, v4
	s_waitcnt lgkmcnt(1)
	s_waitcnt lgkmcnt(0)
	v_mov_b32_e32 v27, v30
	v_mov_b32_e32 v28, v22
	v_mov_b32_e32 v29, v23
	v_lshl_add_u32 v1, v1, 12, v3
	buffer_store_dwordx4 v[26:29], v1, s[36:39], 0 offen sc1
